# phase 3 (low-rank rms norms + rope key) rewritten by hand on top of v28: all rows of a wave in flight
# speedup vs baseline: 1.0025x; 1.0025x over previous
; DEV unsigned cvt_pk_bf16(float lo, float hi) { const f32x2 v = {lo, hi}; const bf16n2 r = __builtin_convertvector(v, bf16n2); return __builtin_bit_cast(unsigned, r); }
; DEV float bflo(unsigned v) { return __uint_as_float(v << 16); }
; DEV float bfhi(unsigned v) { return __uint_as_float(v & 0xffff0000u); }
; DEV void phase3_rows(CParams& p, int wg, int nwg) {
;     ...
;   for (int row = wg * 8 + wid; row < NROW; row += nwg * 8) {
;     if (row >= NCTX) {
;       const int lr = row - NCTX;
;       const u32x4 raw = *(const u32x4*)(p.cq + (long)lr * QRANK + lane * 8);
;       float v[8]; v[0] = bflo(raw.x); v[1] = bfhi(raw.x); v[2] = bflo(raw.y); v[3] = bfhi(raw.y); v[4] = bflo(raw.z); v[5] = bfhi(raw.z); v[6] = bflo(raw.w); v[7] = bfhi(raw.w);
;       float ss = 0.f;
; #pragma unroll
;       for (int j = 0; j < 8; ++j) ss += v[j] * v[j];
;       ss = wave_sum(ss); const float rstd = rsqrtf(ss * (1.f / QRANK) + EPS);
;       const f32x4 w0 = *(const f32x4*)(p.q_norm + lane * 8), w1 = *(const f32x4*)(p.q_norm + lane * 8 + 4);
;       u32x4 o; o.x = cvt_pk_bf16(v[0] * rstd * w0[0], v[1] * rstd * w0[1]); o.y = cvt_pk_bf16(v[2] * rstd * w0[2], v[3] * rstd * w0[3]);
;       o.z = cvt_pk_bf16(v[4] * rstd * w1[0], v[5] * rstd * w1[1]); o.w = cvt_pk_bf16(v[6] * rstd * w1[2], v[7] * rstd * w1[3]);
;       *(u32x4*)(p.cqn + (long)lr * QRANK + lane * 8) = o;
;     }
;     {
;       const u32x2 raw = *(const u32x2*)(p.ckv + (long)row * KVRANK + lane * 4);
;       float v[4]; v[0] = bflo(raw.x); v[1] = bfhi(raw.x); v[2] = bflo(raw.y); v[3] = bfhi(raw.y);
;       float ss = v[0] * v[0] + v[1] * v[1] + v[2] * v[2] + v[3] * v[3];
;       ss = wave_sum(ss); const float rstd = rsqrtf(ss * (1.f / KVRANK) + EPS);
;       const f32x4 w0 = *(const f32x4*)(p.kv_norm + lane * 4);
;       u32x2 o; o.x = cvt_pk_bf16(v[0] * rstd * w0[0], v[1] * rstd * w0[1]); o.y = cvt_pk_bf16(v[2] * rstd * w0[2], v[3] * rstd * w0[3]);
;       *(u32x2*)(p.ckvn + (long)row * KVRANK + lane * 4) = o;
;     }
;     {
;       const float kv = p.kr[(long)row * ROPE + lane];
;       const float other = __shfl_xor(kv, 32);
;       float o = kv;
;       int b, key; row_to_bkey(row, b, key);
;       if (row >= NCTX) {
;         const int t = (row - NCTX) & 4095, a = lane & 31;
;         const float cs = p.rope[t * 64 + a], sn = p.rope[t * 64 + 32 + a];
.LBB0_398:
	s_or_b64 exec, exec, s[4:5]
	s_mov_b64 s[20:21], s[0:1]
	s_waitcnt lgkmcnt(0)
	v_mov_b32_e32 v1, v0
	s_barrier
	s_mov_b64 s[16:17], exec
	s_load_dwordx8 s[4:11], s[0:1], 0x120
	s_load_dwordx2 s[12:13], s[0:1], 0x140
	s_load_dwordx2 s[14:15], s[0:1], 0x110
	s_load_dwordx2 s[18:19], s[0:1], 0x178
	s_load_dwordx4 s[20:23], s[0:1], 0x58
	v_mbcnt_lo_u32_b32 v1, -1, 0
	v_mbcnt_hi_u32_b32 v1, -1, v1
	v_lshlrev_b32_e32 v2, 4, v1
	v_lshlrev_b32_e32 v3, 3, v1
	v_lshlrev_b32_e32 v4, 2, v1
	v_lshlrev_b32_e32 v5, 1, v1
	v_lshlrev_b32_e32 v6, 5, v1
	v_and_b32_e32 v7, 31, v1
	v_lshlrev_b32_e32 v7, 2, v7
	v_xor_b32_e32 v8, 32, v1
	v_lshlrev_b32_e32 v8, 2, v8
	v_xor_b32_e32 v9, 16, v1
	v_lshlrev_b32_e32 v9, 2, v9
	v_xor_b32_e32 v10, 8, v1
	v_lshlrev_b32_e32 v10, 2, v10
	v_xor_b32_e32 v11, 4, v1
	v_lshlrev_b32_e32 v11, 2, v11
	v_xor_b32_e32 v12, 2, v1
	v_lshlrev_b32_e32 v12, 2, v12
	v_xor_b32_e32 v13, 1, v1
	v_lshlrev_b32_e32 v13, 2, v13
	v_cmp_gt_u32_e64 s[24:25], 32, v1
	v_lshrrev_b32_e32 v14, 6, v0
	s_nop 0
	v_readfirstlane_b32 s26, v14
	s_nop 3
	s_add_i32 s26, s75, s26
	s_lshl_b32 s27, s33, 3
	s_waitcnt lgkmcnt(0)
	global_load_dwordx4 v[16:19], v6, s[20:21]
	global_load_dwordx4 v[20:23], v6, s[20:21] offset:16
	global_load_dwordx4 v[24:27], v2, s[22:23]
	s_cmp_lt_u32 s26, 0x4400
	s_cbranch_scc0 .Lp3_end
.Lp3_chunk:
	s_mov_b32 s28, s26
	s_min_u32 s29, s28, 0x43ff
	s_sub_u32 s30, s29, 0x400
	s_max_i32 s30, s30, 0
	s_lshl_b32 s31, s30, 10
	s_add_u32 s52, s4, s31
	s_addc_u32 s53, s5, 0
	global_load_dwordx4 v[28:31], v2, s[52:53]
	s_lshl_b32 s31, s29, 9
	s_add_u32 s52, s8, s31
	s_addc_u32 s53, s9, 0
	global_load_dwordx2 v[32:33], v3, s[52:53]
	s_lshl_b32 s31, s29, 8
	s_add_u32 s52, s12, s31
	s_addc_u32 s53, s13, 0
	global_load_dword v34, v4, s[52:53]
	s_and_b32 s31, s30, 0xfff
	s_lshl_b32 s31, s31, 8
	s_add_u32 s52, s14, s31
	s_addc_u32 s53, s15, 0
	global_load_dword v35, v7, s[52:53]
	global_load_dword v36, v7, s[52:53] offset:128
	s_add_u32 s28, s28, s27
	s_min_u32 s29, s28, 0x43ff
	s_sub_u32 s30, s29, 0x400
	s_max_i32 s30, s30, 0
	s_lshl_b32 s31, s30, 10
	s_add_u32 s52, s4, s31
	s_addc_u32 s53, s5, 0
	global_load_dwordx4 v[38:41], v2, s[52:53]
	s_lshl_b32 s31, s29, 9
	s_add_u32 s52, s8, s31
	s_addc_u32 s53, s9, 0
	global_load_dwordx2 v[42:43], v3, s[52:53]
	s_lshl_b32 s31, s29, 8
	s_add_u32 s52, s12, s31
	s_addc_u32 s53, s13, 0
	global_load_dword v44, v4, s[52:53]
	s_and_b32 s31, s30, 0xfff
	s_lshl_b32 s31, s31, 8
	s_add_u32 s52, s14, s31
	s_addc_u32 s53, s15, 0
	global_load_dword v45, v7, s[52:53]
	global_load_dword v46, v7, s[52:53] offset:128
	s_add_u32 s28, s28, s27
	s_min_u32 s29, s28, 0x43ff
	s_sub_u32 s30, s29, 0x400
	s_max_i32 s30, s30, 0
	s_lshl_b32 s31, s30, 10
	s_add_u32 s52, s4, s31
	s_addc_u32 s53, s5, 0
	global_load_dwordx4 v[48:51], v2, s[52:53]
	s_lshl_b32 s31, s29, 9
	s_add_u32 s52, s8, s31
	s_addc_u32 s53, s9, 0
	global_load_dwordx2 v[52:53], v3, s[52:53]
	s_lshl_b32 s31, s29, 8
	s_add_u32 s52, s12, s31
	s_addc_u32 s53, s13, 0
	global_load_dword v54, v4, s[52:53]
	s_and_b32 s31, s30, 0xfff
	s_lshl_b32 s31, s31, 8
	s_add_u32 s52, s14, s31
	s_addc_u32 s53, s15, 0
	global_load_dword v55, v7, s[52:53]
	global_load_dword v56, v7, s[52:53] offset:128
	s_add_u32 s28, s28, s27
	s_min_u32 s29, s28, 0x43ff
	s_sub_u32 s30, s29, 0x400
	s_max_i32 s30, s30, 0
	s_lshl_b32 s31, s30, 10
	s_add_u32 s52, s4, s31
	s_addc_u32 s53, s5, 0
	global_load_dwordx4 v[58:61], v2, s[52:53]
	s_lshl_b32 s31, s29, 9
	s_add_u32 s52, s8, s31
	s_addc_u32 s53, s9, 0
	global_load_dwordx2 v[62:63], v3, s[52:53]
	s_lshl_b32 s31, s29, 8
	s_add_u32 s52, s12, s31
	s_addc_u32 s53, s13, 0
	global_load_dword v64, v4, s[52:53]
	s_and_b32 s31, s30, 0xfff
	s_lshl_b32 s31, s31, 8
	s_add_u32 s52, s14, s31
	s_addc_u32 s53, s15, 0
	global_load_dword v65, v7, s[52:53]
	global_load_dword v66, v7, s[52:53] offset:128
	s_add_u32 s28, s28, s27
	s_min_u32 s29, s28, 0x43ff
	s_sub_u32 s30, s29, 0x400
	s_max_i32 s30, s30, 0
	s_lshl_b32 s31, s30, 10
	s_add_u32 s52, s4, s31
	s_addc_u32 s53, s5, 0
	global_load_dwordx4 v[68:71], v2, s[52:53]
	s_lshl_b32 s31, s29, 9
	s_add_u32 s52, s8, s31
	s_addc_u32 s53, s9, 0
	global_load_dwordx2 v[72:73], v3, s[52:53]
	s_lshl_b32 s31, s29, 8
	s_add_u32 s52, s12, s31
	s_addc_u32 s53, s13, 0
	global_load_dword v74, v4, s[52:53]
	s_and_b32 s31, s30, 0xfff
	s_lshl_b32 s31, s31, 8
	s_add_u32 s52, s14, s31
	s_addc_u32 s53, s15, 0
	global_load_dword v75, v7, s[52:53]
	global_load_dword v76, v7, s[52:53] offset:128
	s_add_u32 s28, s28, s27
	s_min_u32 s29, s28, 0x43ff
	s_sub_u32 s30, s29, 0x400
	s_max_i32 s30, s30, 0
	s_lshl_b32 s31, s30, 10
	s_add_u32 s52, s4, s31
	s_addc_u32 s53, s5, 0
	global_load_dwordx4 v[78:81], v2, s[52:53]
	s_lshl_b32 s31, s29, 9
	s_add_u32 s52, s8, s31
	s_addc_u32 s53, s9, 0
	global_load_dwordx2 v[82:83], v3, s[52:53]
	s_lshl_b32 s31, s29, 8
	s_add_u32 s52, s12, s31
	s_addc_u32 s53, s13, 0
	global_load_dword v84, v4, s[52:53]
	s_and_b32 s31, s30, 0xfff
	s_lshl_b32 s31, s31, 8
	s_add_u32 s52, s14, s31
	s_addc_u32 s53, s15, 0
	global_load_dword v85, v7, s[52:53]
	global_load_dword v86, v7, s[52:53] offset:128
	s_add_u32 s28, s28, s27
	s_min_u32 s29, s28, 0x43ff
	s_sub_u32 s30, s29, 0x400
	s_max_i32 s30, s30, 0
	s_lshl_b32 s31, s30, 10
	s_add_u32 s52, s4, s31
	s_addc_u32 s53, s5, 0
	global_load_dwordx4 v[88:91], v2, s[52:53]
	s_lshl_b32 s31, s29, 9
	s_add_u32 s52, s8, s31
	s_addc_u32 s53, s9, 0
	global_load_dwordx2 v[92:93], v3, s[52:53]
	s_lshl_b32 s31, s29, 8
	s_add_u32 s52, s12, s31
	s_addc_u32 s53, s13, 0
	global_load_dword v94, v4, s[52:53]
	s_and_b32 s31, s30, 0xfff
	s_lshl_b32 s31, s31, 8
	s_add_u32 s52, s14, s31
	s_addc_u32 s53, s15, 0
; DEV unsigned cvt_pk_bf16(float lo, float hi) { const f32x2 v = {lo, hi}; const bf16n2 r = __builtin_convertvector(v, bf16n2); return __builtin_bit_cast(unsigned, r); }
; DEV float bflo(unsigned v) { return __uint_as_float(v << 16); }
; DEV float bfhi(unsigned v) { return __uint_as_float(v & 0xffff0000u); }
; DEV void phase3_rows(CParams& p, int wg, int nwg) {
;     ...
;     if (row >= NCTX) {
;       const int lr = row - NCTX;
;       const u32x4 raw = *(const u32x4*)(p.cq + (long)lr * QRANK + lane * 8);
;       float v[8]; v[0] = bflo(raw.x); v[1] = bfhi(raw.x); v[2] = bflo(raw.y); v[3] = bfhi(raw.y); v[4] = bflo(raw.z); v[5] = bfhi(raw.z); v[6] = bflo(raw.w); v[7] = bfhi(raw.w);
;       float ss = 0.f;
; #pragma unroll
;       for (int j = 0; j < 8; ++j) ss += v[j] * v[j];
;       ss = wave_sum(ss); const float rstd = rsqrtf(ss * (1.f / QRANK) + EPS);
;       const f32x4 w0 = *(const f32x4*)(p.q_norm + lane * 8), w1 = *(const f32x4*)(p.q_norm + lane * 8 + 4);
;       u32x4 o; o.x = cvt_pk_bf16(v[0] * rstd * w0[0], v[1] * rstd * w0[1]); o.y = cvt_pk_bf16(v[2] * rstd * w0[2], v[3] * rstd * w0[3]);
;       o.z = cvt_pk_bf16(v[4] * rstd * w1[0], v[5] * rstd * w1[1]); o.w = cvt_pk_bf16(v[6] * rstd * w1[2], v[7] * rstd * w1[3]);
;       *(u32x4*)(p.cqn + (long)lr * QRANK + lane * 8) = o;
;     }
;     {
;       const u32x2 raw = *(const u32x2*)(p.ckv + (long)row * KVRANK + lane * 4);
;       float v[4]; v[0] = bflo(raw.x); v[1] = bfhi(raw.x); v[2] = bflo(raw.y); v[3] = bfhi(raw.y);
;       float ss = v[0] * v[0] + v[1] * v[1] + v[2] * v[2] + v[3] * v[3];
;       ss = wave_sum(ss); const float rstd = rsqrtf(ss * (1.f / KVRANK) + EPS);
;       const f32x4 w0 = *(const f32x4*)(p.kv_norm + lane * 4);
;       u32x2 o; o.x = cvt_pk_bf16(v[0] * rstd * w0[0], v[1] * rstd * w0[1]); o.y = cvt_pk_bf16(v[2] * rstd * w0[2], v[3] * rstd * w0[3]);
;       *(u32x2*)(p.ckvn + (long)row * KVRANK + lane * 4) = o;
;     }
;     {
;       const float kv = p.kr[(long)row * ROPE + lane];
;       const float other = __shfl_xor(kv, 32);
;       float o = kv;
;       int b, key; row_to_bkey(row, b, key);
;       if (row >= NCTX) {
;         const int t = (row - NCTX) & 4095, a = lane & 31;
;         const float cs = p.rope[t * 64 + a], sn = p.rope[t * 64 + 32 + a];
;         o = lane < 32 ? kv * cs - other * sn : other * sn + kv * cs;
	global_load_dword v95, v7, s[52:53]
	global_load_dword v96, v7, s[52:53] offset:128
	s_add_u32 s28, s28, s27
	s_min_u32 s29, s28, 0x43ff
	s_sub_u32 s30, s29, 0x400
	s_max_i32 s30, s30, 0
	s_lshl_b32 s31, s30, 10
	s_add_u32 s52, s4, s31
	s_addc_u32 s53, s5, 0
	global_load_dwordx4 v[98:101], v2, s[52:53]
	s_lshl_b32 s31, s29, 9
	s_add_u32 s52, s8, s31
	s_addc_u32 s53, s9, 0
	global_load_dwordx2 v[102:103], v3, s[52:53]
	s_lshl_b32 s31, s29, 8
	s_add_u32 s52, s12, s31
	s_addc_u32 s53, s13, 0
	global_load_dword v104, v4, s[52:53]
	s_and_b32 s31, s30, 0xfff
	s_lshl_b32 s31, s31, 8
	s_add_u32 s52, s14, s31
	s_addc_u32 s53, s15, 0
	global_load_dword v105, v7, s[52:53]
	global_load_dword v106, v7, s[52:53] offset:128
	s_add_u32 s28, s28, s27
	s_min_u32 s29, s28, 0x43ff
	s_sub_u32 s30, s29, 0x400
	s_max_i32 s30, s30, 0
	s_lshl_b32 s31, s30, 10
	s_add_u32 s52, s4, s31
	s_addc_u32 s53, s5, 0
	global_load_dwordx4 v[108:111], v2, s[52:53]
	s_lshl_b32 s31, s29, 9
	s_add_u32 s52, s8, s31
	s_addc_u32 s53, s9, 0
	global_load_dwordx2 v[112:113], v3, s[52:53]
	s_lshl_b32 s31, s29, 8
	s_add_u32 s52, s12, s31
	s_addc_u32 s53, s13, 0
	global_load_dword v114, v4, s[52:53]
	s_and_b32 s31, s30, 0xfff
	s_lshl_b32 s31, s31, 8
	s_add_u32 s52, s14, s31
	s_addc_u32 s53, s15, 0
	global_load_dword v115, v7, s[52:53]
	global_load_dword v116, v7, s[52:53] offset:128
	s_mov_b32 s28, s26
	s_cmp_lt_u32 s28, 0x4400
	s_cbranch_scc0 .Lp3_end
	s_waitcnt vmcnt(40)
	v_lshlrev_b32_e32 v120, 16, v28
	v_and_b32_e32 v121, 0xffff0000, v28
	v_lshlrev_b32_e32 v122, 16, v29
	v_and_b32_e32 v123, 0xffff0000, v29
	v_lshlrev_b32_e32 v124, 16, v30
	v_and_b32_e32 v125, 0xffff0000, v30
	v_lshlrev_b32_e32 v126, 16, v31
	v_and_b32_e32 v127, 0xffff0000, v31
	v_lshlrev_b32_e32 v128, 16, v32
	v_and_b32_e32 v129, 0xffff0000, v32
	v_lshlrev_b32_e32 v130, 16, v33
	v_and_b32_e32 v131, 0xffff0000, v33
	v_mul_f32_e32 v132, v120, v120
	v_fmac_f32_e32 v132, v121, v121
	v_fmac_f32_e32 v132, v122, v122
	v_fmac_f32_e32 v132, v123, v123
	v_fmac_f32_e32 v132, v124, v124
	v_fmac_f32_e32 v132, v125, v125
	v_fmac_f32_e32 v132, v126, v126
	v_fmac_f32_e32 v132, v127, v127
	v_mul_f32_e32 v133, v128, v128
	v_fmac_f32_e32 v133, v129, v129
	v_fmac_f32_e32 v133, v130, v130
	v_fmac_f32_e32 v133, v131, v131
	ds_bpermute_b32 v136, v8, v34
	ds_bpermute_b32 v134, v8, v132
	ds_bpermute_b32 v135, v8, v133
	s_waitcnt lgkmcnt(0)
	v_add_f32_e32 v132, v132, v134
	v_add_f32_e32 v133, v133, v135
	ds_bpermute_b32 v134, v9, v132
	ds_bpermute_b32 v135, v9, v133
	s_waitcnt lgkmcnt(0)
	v_add_f32_e32 v132, v132, v134
	v_add_f32_e32 v133, v133, v135
	ds_bpermute_b32 v134, v10, v132
	ds_bpermute_b32 v135, v10, v133
	s_waitcnt lgkmcnt(0)
	v_add_f32_e32 v132, v132, v134
	v_add_f32_e32 v133, v133, v135
	ds_bpermute_b32 v134, v11, v132
	ds_bpermute_b32 v135, v11, v133
	s_waitcnt lgkmcnt(0)
	v_add_f32_e32 v132, v132, v134
	v_add_f32_e32 v133, v133, v135
	ds_bpermute_b32 v134, v12, v132
	ds_bpermute_b32 v135, v12, v133
	s_waitcnt lgkmcnt(0)
	v_add_f32_e32 v132, v132, v134
	v_add_f32_e32 v133, v133, v135
	ds_bpermute_b32 v134, v13, v132
	ds_bpermute_b32 v135, v13, v133
	s_waitcnt lgkmcnt(0)
	v_add_f32_e32 v132, v132, v134
	v_add_f32_e32 v133, v133, v135
	v_mov_b32_e32 v134, 0x358637bd
	v_mov_b32_e32 v135, 0x358637bd
	v_fmac_f32_e32 v134, 0x3b000000, v132
	v_fmac_f32_e32 v135, 0x3b800000, v133
	v_rsq_f32_e32 v134, v134
	v_rsq_f32_e32 v135, v135
	s_sub_u32 s30, s28, 0x400
	s_cmp_lt_i32 s30, 0
	s_cbranch_scc1 .Lp3_ctx0
	v_mul_f32_e32 v120, v120, v134
	v_mul_f32_e32 v120, v120, v16
	v_mul_f32_e32 v121, v121, v134
	v_mul_f32_e32 v121, v121, v17
	v_mul_f32_e32 v122, v122, v134
	v_mul_f32_e32 v122, v122, v18
	v_mul_f32_e32 v123, v123, v134
	v_mul_f32_e32 v123, v123, v19
	v_mul_f32_e32 v124, v124, v134
	v_mul_f32_e32 v124, v124, v20
	v_mul_f32_e32 v125, v125, v134
	v_mul_f32_e32 v125, v125, v21
	v_mul_f32_e32 v126, v126, v134
	v_mul_f32_e32 v126, v126, v22
	v_mul_f32_e32 v127, v127, v134
	v_mul_f32_e32 v127, v127, v23
	v_cvt_pk_bf16_f32 v140, v120, v121
	v_cvt_pk_bf16_f32 v141, v122, v123
	v_cvt_pk_bf16_f32 v142, v124, v125
	v_cvt_pk_bf16_f32 v143, v126, v127
	s_lshl_b32 s31, s30, 10
	s_add_u32 s52, s6, s31
	s_addc_u32 s53, s7, 0
	global_store_dwordx4 v2, v[140:143], s[52:53]
	v_mul_f32_e32 v137, v136, v36
	v_fma_f32 v138, v34, v35, -v137
	v_fma_f32 v139, v34, v35, v137
	v_cndmask_b32_e64 v138, v139, v138, s[24:25]
	s_lshr_b32 s54, s30, 12
	s_and_b32 s55, s30, 0xfff
	s_add_u32 s55, s55, 0x100
	s_branch .Lp3_kf0
.Lp3_ctx0:
	v_mov_b32_e32 v138, v34
	s_lshr_b32 s54, s28, 8
	s_and_b32 s55, s28, 0xff
; DEV float bflo(unsigned v) { return __uint_as_float(v << 16); }
; DEV float bfhi(unsigned v) { return __uint_as_float(v & 0xffff0000u); }
; DEV void phase3_rows(CParams& p, int wg, int nwg) {
;     ...
;     if (row >= NCTX) {
;       const int lr = row - NCTX;
;       const u32x4 raw = *(const u32x4*)(p.cq + (long)lr * QRANK + lane * 8);
;       float v[8]; v[0] = bflo(raw.x); v[1] = bfhi(raw.x); v[2] = bflo(raw.y); v[3] = bfhi(raw.y); v[4] = bflo(raw.z); v[5] = bfhi(raw.z); v[6] = bflo(raw.w); v[7] = bfhi(raw.w);
;       float ss = 0.f;
; #pragma unroll
;       for (int j = 0; j < 8; ++j) ss += v[j] * v[j];
;       ss = wave_sum(ss); const float rstd = rsqrtf(ss * (1.f / QRANK) + EPS);
;       const f32x4 w0 = *(const f32x4*)(p.q_norm + lane * 8), w1 = *(const f32x4*)(p.q_norm + lane * 8 + 4);
;       u32x4 o; o.x = cvt_pk_bf16(v[0] * rstd * w0[0], v[1] * rstd * w0[1]); o.y = cvt_pk_bf16(v[2] * rstd * w0[2], v[3] * rstd * w0[3]);
;       o.z = cvt_pk_bf16(v[4] * rstd * w1[0], v[5] * rstd * w1[1]); o.w = cvt_pk_bf16(v[6] * rstd * w1[2], v[7] * rstd * w1[3]);
;       *(u32x4*)(p.cqn + (long)lr * QRANK + lane * 8) = o;
;     }
;     {
;       const u32x2 raw = *(const u32x2*)(p.ckv + (long)row * KVRANK + lane * 4);
;       float v[4]; v[0] = bflo(raw.x); v[1] = bfhi(raw.x); v[2] = bflo(raw.y); v[3] = bfhi(raw.y);
;       float ss = v[0] * v[0] + v[1] * v[1] + v[2] * v[2] + v[3] * v[3];
;       ss = wave_sum(ss); const float rstd = rsqrtf(ss * (1.f / KVRANK) + EPS);
;       const f32x4 w0 = *(const f32x4*)(p.kv_norm + lane * 4);
;       u32x2 o; o.x = cvt_pk_bf16(v[0] * rstd * w0[0], v[1] * rstd * w0[1]); o.y = cvt_pk_bf16(v[2] * rstd * w0[2], v[3] * rstd * w0[3]);
;       *(u32x2*)(p.ckvn + (long)row * KVRANK + lane * 4) = o;
;     }
;     {
;       const float kv = p.kr[(long)row * ROPE + lane];
;       const float other = __shfl_xor(kv, 32);
;       float o = kv;
;       int b, key; row_to_bkey(row, b, key);
;       if (row >= NCTX) {
;         const int t = (row - NCTX) & 4095, a = lane & 31;
;         const float cs = p.rope[t * 64 + a], sn = p.rope[t * 64 + 32 + a];
;         o = lane < 32 ? kv * cs - other * sn : other * sn + kv * cs;
;       }
;       bf16_t* kd = p.kf + ((long)(b * NH) * KEYS + key) * QK + 128 + lane; const bf16_t ob = f2bf(o);
; #pragma unroll
;       for (int hh = 0; hh < NH; ++hh) kd[(long)hh * KEYS * QK] = ob;
.Lp3_kf0:
	v_mul_f32_e32 v128, v128, v135
	v_mul_f32_e32 v128, v128, v24
	v_mul_f32_e32 v129, v129, v135
	v_mul_f32_e32 v129, v129, v25
	v_mul_f32_e32 v130, v130, v135
	v_mul_f32_e32 v130, v130, v26
	v_mul_f32_e32 v131, v131, v135
	v_mul_f32_e32 v131, v131, v27
	v_cvt_pk_bf16_f32 v144, v128, v129
	v_cvt_pk_bf16_f32 v145, v130, v131
	s_lshl_b32 s31, s28, 9
	s_add_u32 s52, s10, s31
	s_addc_u32 s53, s11, 0
	global_store_dwordx2 v3, v[144:145], s[52:53]
	v_cvt_pk_bf16_f32 v146, v138, v138
	s_mul_i32 s54, s54, 0x8800
	s_add_u32 s54, s54, s55
	s_mul_i32 s54, s54, 0x180
	s_add_u32 s54, s54, 0x100
	s_add_u32 s52, s18, s54
	s_addc_u32 s53, s19, 0
	global_store_short v5, v146, s[52:53]
	s_add_u32 s52, s52, 0x198000
	s_addc_u32 s53, s53, 0
	global_store_short v5, v146, s[52:53]
	s_add_u32 s52, s52, 0x198000
	s_addc_u32 s53, s53, 0
	global_store_short v5, v146, s[52:53]
	s_add_u32 s52, s52, 0x198000
	s_addc_u32 s53, s53, 0
	global_store_short v5, v146, s[52:53]
	s_add_u32 s52, s52, 0x198000
	s_addc_u32 s53, s53, 0
	global_store_short v5, v146, s[52:53]
	s_add_u32 s52, s52, 0x198000
	s_addc_u32 s53, s53, 0
	global_store_short v5, v146, s[52:53]
	s_add_u32 s52, s52, 0x198000
	s_addc_u32 s53, s53, 0
	global_store_short v5, v146, s[52:53]
	s_add_u32 s52, s52, 0x198000
	s_addc_u32 s53, s53, 0
	global_store_short v5, v146, s[52:53]
	s_add_u32 s28, s28, s27
	s_cmp_lt_u32 s28, 0x4400
	s_cbranch_scc0 .Lp3_end
	s_waitcnt vmcnt(44)
	v_lshlrev_b32_e32 v120, 16, v38
	v_and_b32_e32 v121, 0xffff0000, v38
	v_lshlrev_b32_e32 v122, 16, v39
	v_and_b32_e32 v123, 0xffff0000, v39
	v_lshlrev_b32_e32 v124, 16, v40
	v_and_b32_e32 v125, 0xffff0000, v40
	v_lshlrev_b32_e32 v126, 16, v41
	v_and_b32_e32 v127, 0xffff0000, v41
	v_lshlrev_b32_e32 v128, 16, v42
	v_and_b32_e32 v129, 0xffff0000, v42
	v_lshlrev_b32_e32 v130, 16, v43
	v_and_b32_e32 v131, 0xffff0000, v43
	v_mul_f32_e32 v132, v120, v120
	v_fmac_f32_e32 v132, v121, v121
	v_fmac_f32_e32 v132, v122, v122
	v_fmac_f32_e32 v132, v123, v123
	v_fmac_f32_e32 v132, v124, v124
	v_fmac_f32_e32 v132, v125, v125
	v_fmac_f32_e32 v132, v126, v126
	v_fmac_f32_e32 v132, v127, v127
	v_mul_f32_e32 v133, v128, v128
	v_fmac_f32_e32 v133, v129, v129
	v_fmac_f32_e32 v133, v130, v130
	v_fmac_f32_e32 v133, v131, v131
	ds_bpermute_b32 v136, v8, v44
	ds_bpermute_b32 v134, v8, v132
	ds_bpermute_b32 v135, v8, v133
	s_waitcnt lgkmcnt(0)
	v_add_f32_e32 v132, v132, v134
	v_add_f32_e32 v133, v133, v135
	ds_bpermute_b32 v134, v9, v132
	ds_bpermute_b32 v135, v9, v133
	s_waitcnt lgkmcnt(0)
	v_add_f32_e32 v132, v132, v134
	v_add_f32_e32 v133, v133, v135
	ds_bpermute_b32 v134, v10, v132
	ds_bpermute_b32 v135, v10, v133
	s_waitcnt lgkmcnt(0)
	v_add_f32_e32 v132, v132, v134
	v_add_f32_e32 v133, v133, v135
	ds_bpermute_b32 v134, v11, v132
	ds_bpermute_b32 v135, v11, v133
	s_waitcnt lgkmcnt(0)
	v_add_f32_e32 v132, v132, v134
	v_add_f32_e32 v133, v133, v135
	ds_bpermute_b32 v134, v12, v132
	ds_bpermute_b32 v135, v12, v133
	s_waitcnt lgkmcnt(0)
	v_add_f32_e32 v132, v132, v134
	v_add_f32_e32 v133, v133, v135
	ds_bpermute_b32 v134, v13, v132
	ds_bpermute_b32 v135, v13, v133
	s_waitcnt lgkmcnt(0)
	v_add_f32_e32 v132, v132, v134
	v_add_f32_e32 v133, v133, v135
	v_mov_b32_e32 v134, 0x358637bd
	v_mov_b32_e32 v135, 0x358637bd
	v_fmac_f32_e32 v134, 0x3b000000, v132
	v_fmac_f32_e32 v135, 0x3b800000, v133
	v_rsq_f32_e32 v134, v134
	v_rsq_f32_e32 v135, v135
	s_sub_u32 s30, s28, 0x400
	s_cmp_lt_i32 s30, 0
	s_cbranch_scc1 .Lp3_ctx1
	v_mul_f32_e32 v120, v120, v134
	v_mul_f32_e32 v120, v120, v16
	v_mul_f32_e32 v121, v121, v134
	v_mul_f32_e32 v121, v121, v17
	v_mul_f32_e32 v122, v122, v134
	v_mul_f32_e32 v122, v122, v18
	v_mul_f32_e32 v123, v123, v134
	v_mul_f32_e32 v123, v123, v19
	v_mul_f32_e32 v124, v124, v134
	v_mul_f32_e32 v124, v124, v20
	v_mul_f32_e32 v125, v125, v134
	v_mul_f32_e32 v125, v125, v21
	v_mul_f32_e32 v126, v126, v134
	v_mul_f32_e32 v126, v126, v22
	v_mul_f32_e32 v127, v127, v134
	v_mul_f32_e32 v127, v127, v23
	v_cvt_pk_bf16_f32 v140, v120, v121
	v_cvt_pk_bf16_f32 v141, v122, v123
	v_cvt_pk_bf16_f32 v142, v124, v125
	v_cvt_pk_bf16_f32 v143, v126, v127
	s_lshl_b32 s31, s30, 10
	s_add_u32 s52, s6, s31
	s_addc_u32 s53, s7, 0
	global_store_dwordx4 v2, v[140:143], s[52:53]
	v_mul_f32_e32 v137, v136, v46
	v_fma_f32 v138, v44, v45, -v137
	v_fma_f32 v139, v44, v45, v137
	v_cndmask_b32_e64 v138, v139, v138, s[24:25]
	s_lshr_b32 s54, s30, 12
	s_and_b32 s55, s30, 0xfff
	s_add_u32 s55, s55, 0x100
	s_branch .Lp3_kf1
.Lp3_ctx1:
	v_mov_b32_e32 v138, v44
	s_lshr_b32 s54, s28, 8
	s_and_b32 s55, s28, 0xff
; DEV float bflo(unsigned v) { return __uint_as_float(v << 16); }
; DEV float bfhi(unsigned v) { return __uint_as_float(v & 0xffff0000u); }
; DEV void phase3_rows(CParams& p, int wg, int nwg) {
;     ...
;     if (row >= NCTX) {
;       const int lr = row - NCTX;
;       const u32x4 raw = *(const u32x4*)(p.cq + (long)lr * QRANK + lane * 8);
;       float v[8]; v[0] = bflo(raw.x); v[1] = bfhi(raw.x); v[2] = bflo(raw.y); v[3] = bfhi(raw.y); v[4] = bflo(raw.z); v[5] = bfhi(raw.z); v[6] = bflo(raw.w); v[7] = bfhi(raw.w);
;       float ss = 0.f;
; #pragma unroll
;       for (int j = 0; j < 8; ++j) ss += v[j] * v[j];
;       ss = wave_sum(ss); const float rstd = rsqrtf(ss * (1.f / QRANK) + EPS);
;       const f32x4 w0 = *(const f32x4*)(p.q_norm + lane * 8), w1 = *(const f32x4*)(p.q_norm + lane * 8 + 4);
;       u32x4 o; o.x = cvt_pk_bf16(v[0] * rstd * w0[0], v[1] * rstd * w0[1]); o.y = cvt_pk_bf16(v[2] * rstd * w0[2], v[3] * rstd * w0[3]);
;       o.z = cvt_pk_bf16(v[4] * rstd * w1[0], v[5] * rstd * w1[1]); o.w = cvt_pk_bf16(v[6] * rstd * w1[2], v[7] * rstd * w1[3]);
;       *(u32x4*)(p.cqn + (long)lr * QRANK + lane * 8) = o;
;     }
;     {
;       const u32x2 raw = *(const u32x2*)(p.ckv + (long)row * KVRANK + lane * 4);
;       float v[4]; v[0] = bflo(raw.x); v[1] = bfhi(raw.x); v[2] = bflo(raw.y); v[3] = bfhi(raw.y);
;       float ss = v[0] * v[0] + v[1] * v[1] + v[2] * v[2] + v[3] * v[3];
;       ss = wave_sum(ss); const float rstd = rsqrtf(ss * (1.f / KVRANK) + EPS);
;       const f32x4 w0 = *(const f32x4*)(p.kv_norm + lane * 4);
;       u32x2 o; o.x = cvt_pk_bf16(v[0] * rstd * w0[0], v[1] * rstd * w0[1]); o.y = cvt_pk_bf16(v[2] * rstd * w0[2], v[3] * rstd * w0[3]);
;       *(u32x2*)(p.ckvn + (long)row * KVRANK + lane * 4) = o;
;     }
;     {
;       const float kv = p.kr[(long)row * ROPE + lane];
;       const float other = __shfl_xor(kv, 32);
;       float o = kv;
;       int b, key; row_to_bkey(row, b, key);
;       if (row >= NCTX) {
;         const int t = (row - NCTX) & 4095, a = lane & 31;
;         const float cs = p.rope[t * 64 + a], sn = p.rope[t * 64 + 32 + a];
;         o = lane < 32 ? kv * cs - other * sn : other * sn + kv * cs;
;       }
;       bf16_t* kd = p.kf + ((long)(b * NH) * KEYS + key) * QK + 128 + lane; const bf16_t ob = f2bf(o);
; #pragma unroll
;       for (int hh = 0; hh < NH; ++hh) kd[(long)hh * KEYS * QK] = ob;
.Lp3_kf1:
	v_mul_f32_e32 v128, v128, v135
	v_mul_f32_e32 v128, v128, v24
	v_mul_f32_e32 v129, v129, v135
	v_mul_f32_e32 v129, v129, v25
	v_mul_f32_e32 v130, v130, v135
	v_mul_f32_e32 v130, v130, v26
	v_mul_f32_e32 v131, v131, v135
	v_mul_f32_e32 v131, v131, v27
	v_cvt_pk_bf16_f32 v144, v128, v129
	v_cvt_pk_bf16_f32 v145, v130, v131
	s_lshl_b32 s31, s28, 9
	s_add_u32 s52, s10, s31
	s_addc_u32 s53, s11, 0
	global_store_dwordx2 v3, v[144:145], s[52:53]
	v_cvt_pk_bf16_f32 v146, v138, v138
	s_mul_i32 s54, s54, 0x8800
	s_add_u32 s54, s54, s55
	s_mul_i32 s54, s54, 0x180
	s_add_u32 s54, s54, 0x100
	s_add_u32 s52, s18, s54
	s_addc_u32 s53, s19, 0
	global_store_short v5, v146, s[52:53]
	s_add_u32 s52, s52, 0x198000
	s_addc_u32 s53, s53, 0
	global_store_short v5, v146, s[52:53]
	s_add_u32 s52, s52, 0x198000
	s_addc_u32 s53, s53, 0
	global_store_short v5, v146, s[52:53]
	s_add_u32 s52, s52, 0x198000
	s_addc_u32 s53, s53, 0
	global_store_short v5, v146, s[52:53]
	s_add_u32 s52, s52, 0x198000
	s_addc_u32 s53, s53, 0
	global_store_short v5, v146, s[52:53]
	s_add_u32 s52, s52, 0x198000
	s_addc_u32 s53, s53, 0
	global_store_short v5, v146, s[52:53]
	s_add_u32 s52, s52, 0x198000
	s_addc_u32 s53, s53, 0
	global_store_short v5, v146, s[52:53]
	s_add_u32 s52, s52, 0x198000
	s_addc_u32 s53, s53, 0
	global_store_short v5, v146, s[52:53]
	s_add_u32 s28, s28, s27
	s_cmp_lt_u32 s28, 0x4400
	s_cbranch_scc0 .Lp3_end
	s_waitcnt vmcnt(48)
	v_lshlrev_b32_e32 v120, 16, v48
	v_and_b32_e32 v121, 0xffff0000, v48
	v_lshlrev_b32_e32 v122, 16, v49
	v_and_b32_e32 v123, 0xffff0000, v49
	v_lshlrev_b32_e32 v124, 16, v50
	v_and_b32_e32 v125, 0xffff0000, v50
	v_lshlrev_b32_e32 v126, 16, v51
	v_and_b32_e32 v127, 0xffff0000, v51
	v_lshlrev_b32_e32 v128, 16, v52
	v_and_b32_e32 v129, 0xffff0000, v52
	v_lshlrev_b32_e32 v130, 16, v53
	v_and_b32_e32 v131, 0xffff0000, v53
	v_mul_f32_e32 v132, v120, v120
	v_fmac_f32_e32 v132, v121, v121
	v_fmac_f32_e32 v132, v122, v122
	v_fmac_f32_e32 v132, v123, v123
	v_fmac_f32_e32 v132, v124, v124
	v_fmac_f32_e32 v132, v125, v125
	v_fmac_f32_e32 v132, v126, v126
	v_fmac_f32_e32 v132, v127, v127
	v_mul_f32_e32 v133, v128, v128
	v_fmac_f32_e32 v133, v129, v129
	v_fmac_f32_e32 v133, v130, v130
	v_fmac_f32_e32 v133, v131, v131
	ds_bpermute_b32 v136, v8, v54
	ds_bpermute_b32 v134, v8, v132
	ds_bpermute_b32 v135, v8, v133
	s_waitcnt lgkmcnt(0)
	v_add_f32_e32 v132, v132, v134
	v_add_f32_e32 v133, v133, v135
	ds_bpermute_b32 v134, v9, v132
	ds_bpermute_b32 v135, v9, v133
	s_waitcnt lgkmcnt(0)
	v_add_f32_e32 v132, v132, v134
	v_add_f32_e32 v133, v133, v135
	ds_bpermute_b32 v134, v10, v132
	ds_bpermute_b32 v135, v10, v133
	s_waitcnt lgkmcnt(0)
	v_add_f32_e32 v132, v132, v134
	v_add_f32_e32 v133, v133, v135
	ds_bpermute_b32 v134, v11, v132
	ds_bpermute_b32 v135, v11, v133
	s_waitcnt lgkmcnt(0)
	v_add_f32_e32 v132, v132, v134
	v_add_f32_e32 v133, v133, v135
	ds_bpermute_b32 v134, v12, v132
	ds_bpermute_b32 v135, v12, v133
	s_waitcnt lgkmcnt(0)
	v_add_f32_e32 v132, v132, v134
	v_add_f32_e32 v133, v133, v135
	ds_bpermute_b32 v134, v13, v132
	ds_bpermute_b32 v135, v13, v133
	s_waitcnt lgkmcnt(0)
	v_add_f32_e32 v132, v132, v134
	v_add_f32_e32 v133, v133, v135
	v_mov_b32_e32 v134, 0x358637bd
	v_mov_b32_e32 v135, 0x358637bd
	v_fmac_f32_e32 v134, 0x3b000000, v132
	v_fmac_f32_e32 v135, 0x3b800000, v133
	v_rsq_f32_e32 v134, v134
	v_rsq_f32_e32 v135, v135
	s_sub_u32 s30, s28, 0x400
	s_cmp_lt_i32 s30, 0
	s_cbranch_scc1 .Lp3_ctx2
	v_mul_f32_e32 v120, v120, v134
	v_mul_f32_e32 v120, v120, v16
	v_mul_f32_e32 v121, v121, v134
	v_mul_f32_e32 v121, v121, v17
	v_mul_f32_e32 v122, v122, v134
	v_mul_f32_e32 v122, v122, v18
	v_mul_f32_e32 v123, v123, v134
	v_mul_f32_e32 v123, v123, v19
	v_mul_f32_e32 v124, v124, v134
	v_mul_f32_e32 v124, v124, v20
	v_mul_f32_e32 v125, v125, v134
	v_mul_f32_e32 v125, v125, v21
	v_mul_f32_e32 v126, v126, v134
	v_mul_f32_e32 v126, v126, v22
	v_mul_f32_e32 v127, v127, v134
	v_mul_f32_e32 v127, v127, v23
	v_cvt_pk_bf16_f32 v140, v120, v121
	v_cvt_pk_bf16_f32 v141, v122, v123
	v_cvt_pk_bf16_f32 v142, v124, v125
	v_cvt_pk_bf16_f32 v143, v126, v127
	s_lshl_b32 s31, s30, 10
	s_add_u32 s52, s6, s31
	s_addc_u32 s53, s7, 0
	global_store_dwordx4 v2, v[140:143], s[52:53]
	v_mul_f32_e32 v137, v136, v56
	v_fma_f32 v138, v54, v55, -v137
	v_fma_f32 v139, v54, v55, v137
	v_cndmask_b32_e64 v138, v139, v138, s[24:25]
	s_lshr_b32 s54, s30, 12
	s_and_b32 s55, s30, 0xfff
	s_add_u32 s55, s55, 0x100
	s_branch .Lp3_kf2
.Lp3_ctx2:
	v_mov_b32_e32 v138, v54
	s_lshr_b32 s54, s28, 8
	s_and_b32 s55, s28, 0xff
; DEV float bflo(unsigned v) { return __uint_as_float(v << 16); }
; DEV float bfhi(unsigned v) { return __uint_as_float(v & 0xffff0000u); }
; DEV void phase3_rows(CParams& p, int wg, int nwg) {
;     ...
;     if (row >= NCTX) {
;       const int lr = row - NCTX;
;       const u32x4 raw = *(const u32x4*)(p.cq + (long)lr * QRANK + lane * 8);
;       float v[8]; v[0] = bflo(raw.x); v[1] = bfhi(raw.x); v[2] = bflo(raw.y); v[3] = bfhi(raw.y); v[4] = bflo(raw.z); v[5] = bfhi(raw.z); v[6] = bflo(raw.w); v[7] = bfhi(raw.w);
;       float ss = 0.f;
; #pragma unroll
;       for (int j = 0; j < 8; ++j) ss += v[j] * v[j];
;       ss = wave_sum(ss); const float rstd = rsqrtf(ss * (1.f / QRANK) + EPS);
;       const f32x4 w0 = *(const f32x4*)(p.q_norm + lane * 8), w1 = *(const f32x4*)(p.q_norm + lane * 8 + 4);
;       u32x4 o; o.x = cvt_pk_bf16(v[0] * rstd * w0[0], v[1] * rstd * w0[1]); o.y = cvt_pk_bf16(v[2] * rstd * w0[2], v[3] * rstd * w0[3]);
;       o.z = cvt_pk_bf16(v[4] * rstd * w1[0], v[5] * rstd * w1[1]); o.w = cvt_pk_bf16(v[6] * rstd * w1[2], v[7] * rstd * w1[3]);
;       *(u32x4*)(p.cqn + (long)lr * QRANK + lane * 8) = o;
;     }
;     {
;       const u32x2 raw = *(const u32x2*)(p.ckv + (long)row * KVRANK + lane * 4);
;       float v[4]; v[0] = bflo(raw.x); v[1] = bfhi(raw.x); v[2] = bflo(raw.y); v[3] = bfhi(raw.y);
;       float ss = v[0] * v[0] + v[1] * v[1] + v[2] * v[2] + v[3] * v[3];
;       ss = wave_sum(ss); const float rstd = rsqrtf(ss * (1.f / KVRANK) + EPS);
;       const f32x4 w0 = *(const f32x4*)(p.kv_norm + lane * 4);
;       u32x2 o; o.x = cvt_pk_bf16(v[0] * rstd * w0[0], v[1] * rstd * w0[1]); o.y = cvt_pk_bf16(v[2] * rstd * w0[2], v[3] * rstd * w0[3]);
;       *(u32x2*)(p.ckvn + (long)row * KVRANK + lane * 4) = o;
;     }
;     {
;       const float kv = p.kr[(long)row * ROPE + lane];
;       const float other = __shfl_xor(kv, 32);
;       float o = kv;
;       int b, key; row_to_bkey(row, b, key);
;       if (row >= NCTX) {
;         const int t = (row - NCTX) & 4095, a = lane & 31;
;         const float cs = p.rope[t * 64 + a], sn = p.rope[t * 64 + 32 + a];
;         o = lane < 32 ? kv * cs - other * sn : other * sn + kv * cs;
;       }
;       bf16_t* kd = p.kf + ((long)(b * NH) * KEYS + key) * QK + 128 + lane; const bf16_t ob = f2bf(o);
; #pragma unroll
;       for (int hh = 0; hh < NH; ++hh) kd[(long)hh * KEYS * QK] = ob;
.Lp3_kf2:
	v_mul_f32_e32 v128, v128, v135
	v_mul_f32_e32 v128, v128, v24
	v_mul_f32_e32 v129, v129, v135
	v_mul_f32_e32 v129, v129, v25
	v_mul_f32_e32 v130, v130, v135
	v_mul_f32_e32 v130, v130, v26
	v_mul_f32_e32 v131, v131, v135
	v_mul_f32_e32 v131, v131, v27
	v_cvt_pk_bf16_f32 v144, v128, v129
	v_cvt_pk_bf16_f32 v145, v130, v131
	s_lshl_b32 s31, s28, 9
	s_add_u32 s52, s10, s31
	s_addc_u32 s53, s11, 0
	global_store_dwordx2 v3, v[144:145], s[52:53]
	v_cvt_pk_bf16_f32 v146, v138, v138
	s_mul_i32 s54, s54, 0x8800
	s_add_u32 s54, s54, s55
	s_mul_i32 s54, s54, 0x180
	s_add_u32 s54, s54, 0x100
	s_add_u32 s52, s18, s54
	s_addc_u32 s53, s19, 0
	global_store_short v5, v146, s[52:53]
	s_add_u32 s52, s52, 0x198000
	s_addc_u32 s53, s53, 0
	global_store_short v5, v146, s[52:53]
	s_add_u32 s52, s52, 0x198000
	s_addc_u32 s53, s53, 0
	global_store_short v5, v146, s[52:53]
	s_add_u32 s52, s52, 0x198000
	s_addc_u32 s53, s53, 0
	global_store_short v5, v146, s[52:53]
	s_add_u32 s52, s52, 0x198000
	s_addc_u32 s53, s53, 0
	global_store_short v5, v146, s[52:53]
	s_add_u32 s52, s52, 0x198000
	s_addc_u32 s53, s53, 0
	global_store_short v5, v146, s[52:53]
	s_add_u32 s52, s52, 0x198000
	s_addc_u32 s53, s53, 0
	global_store_short v5, v146, s[52:53]
	s_add_u32 s52, s52, 0x198000
	s_addc_u32 s53, s53, 0
	global_store_short v5, v146, s[52:53]
	s_add_u32 s28, s28, s27
	s_cmp_lt_u32 s28, 0x4400
	s_cbranch_scc0 .Lp3_end
	s_waitcnt vmcnt(52)
	v_lshlrev_b32_e32 v120, 16, v58
	v_and_b32_e32 v121, 0xffff0000, v58
	v_lshlrev_b32_e32 v122, 16, v59
	v_and_b32_e32 v123, 0xffff0000, v59
	v_lshlrev_b32_e32 v124, 16, v60
	v_and_b32_e32 v125, 0xffff0000, v60
	v_lshlrev_b32_e32 v126, 16, v61
	v_and_b32_e32 v127, 0xffff0000, v61
	v_lshlrev_b32_e32 v128, 16, v62
	v_and_b32_e32 v129, 0xffff0000, v62
	v_lshlrev_b32_e32 v130, 16, v63
	v_and_b32_e32 v131, 0xffff0000, v63
	v_mul_f32_e32 v132, v120, v120
	v_fmac_f32_e32 v132, v121, v121
	v_fmac_f32_e32 v132, v122, v122
	v_fmac_f32_e32 v132, v123, v123
	v_fmac_f32_e32 v132, v124, v124
	v_fmac_f32_e32 v132, v125, v125
	v_fmac_f32_e32 v132, v126, v126
	v_fmac_f32_e32 v132, v127, v127
	v_mul_f32_e32 v133, v128, v128
	v_fmac_f32_e32 v133, v129, v129
	v_fmac_f32_e32 v133, v130, v130
	v_fmac_f32_e32 v133, v131, v131
	ds_bpermute_b32 v136, v8, v64
	ds_bpermute_b32 v134, v8, v132
	ds_bpermute_b32 v135, v8, v133
	s_waitcnt lgkmcnt(0)
	v_add_f32_e32 v132, v132, v134
	v_add_f32_e32 v133, v133, v135
	ds_bpermute_b32 v134, v9, v132
	ds_bpermute_b32 v135, v9, v133
	s_waitcnt lgkmcnt(0)
	v_add_f32_e32 v132, v132, v134
	v_add_f32_e32 v133, v133, v135
	ds_bpermute_b32 v134, v10, v132
	ds_bpermute_b32 v135, v10, v133
	s_waitcnt lgkmcnt(0)
	v_add_f32_e32 v132, v132, v134
	v_add_f32_e32 v133, v133, v135
	ds_bpermute_b32 v134, v11, v132
	ds_bpermute_b32 v135, v11, v133
	s_waitcnt lgkmcnt(0)
	v_add_f32_e32 v132, v132, v134
	v_add_f32_e32 v133, v133, v135
	ds_bpermute_b32 v134, v12, v132
	ds_bpermute_b32 v135, v12, v133
	s_waitcnt lgkmcnt(0)
	v_add_f32_e32 v132, v132, v134
	v_add_f32_e32 v133, v133, v135
	ds_bpermute_b32 v134, v13, v132
	ds_bpermute_b32 v135, v13, v133
	s_waitcnt lgkmcnt(0)
	v_add_f32_e32 v132, v132, v134
	v_add_f32_e32 v133, v133, v135
	v_mov_b32_e32 v134, 0x358637bd
	v_mov_b32_e32 v135, 0x358637bd
	v_fmac_f32_e32 v134, 0x3b000000, v132
	v_fmac_f32_e32 v135, 0x3b800000, v133
	v_rsq_f32_e32 v134, v134
	v_rsq_f32_e32 v135, v135
	s_sub_u32 s30, s28, 0x400
	s_cmp_lt_i32 s30, 0
	s_cbranch_scc1 .Lp3_ctx3
	v_mul_f32_e32 v120, v120, v134
	v_mul_f32_e32 v120, v120, v16
	v_mul_f32_e32 v121, v121, v134
	v_mul_f32_e32 v121, v121, v17
	v_mul_f32_e32 v122, v122, v134
	v_mul_f32_e32 v122, v122, v18
	v_mul_f32_e32 v123, v123, v134
	v_mul_f32_e32 v123, v123, v19
	v_mul_f32_e32 v124, v124, v134
	v_mul_f32_e32 v124, v124, v20
	v_mul_f32_e32 v125, v125, v134
	v_mul_f32_e32 v125, v125, v21
	v_mul_f32_e32 v126, v126, v134
	v_mul_f32_e32 v126, v126, v22
	v_mul_f32_e32 v127, v127, v134
	v_mul_f32_e32 v127, v127, v23
	v_cvt_pk_bf16_f32 v140, v120, v121
	v_cvt_pk_bf16_f32 v141, v122, v123
	v_cvt_pk_bf16_f32 v142, v124, v125
	v_cvt_pk_bf16_f32 v143, v126, v127
	s_lshl_b32 s31, s30, 10
	s_add_u32 s52, s6, s31
	s_addc_u32 s53, s7, 0
	global_store_dwordx4 v2, v[140:143], s[52:53]
	v_mul_f32_e32 v137, v136, v66
	v_fma_f32 v138, v64, v65, -v137
	v_fma_f32 v139, v64, v65, v137
	v_cndmask_b32_e64 v138, v139, v138, s[24:25]
	s_lshr_b32 s54, s30, 12
	s_and_b32 s55, s30, 0xfff
	s_add_u32 s55, s55, 0x100
	s_branch .Lp3_kf3
.Lp3_ctx3:
	v_mov_b32_e32 v138, v64
	s_lshr_b32 s54, s28, 8
	s_and_b32 s55, s28, 0xff
; DEV float bflo(unsigned v) { return __uint_as_float(v << 16); }
; DEV float bfhi(unsigned v) { return __uint_as_float(v & 0xffff0000u); }
; DEV void phase3_rows(CParams& p, int wg, int nwg) {
;     ...
;     if (row >= NCTX) {
;       const int lr = row - NCTX;
;       const u32x4 raw = *(const u32x4*)(p.cq + (long)lr * QRANK + lane * 8);
;       float v[8]; v[0] = bflo(raw.x); v[1] = bfhi(raw.x); v[2] = bflo(raw.y); v[3] = bfhi(raw.y); v[4] = bflo(raw.z); v[5] = bfhi(raw.z); v[6] = bflo(raw.w); v[7] = bfhi(raw.w);
;       float ss = 0.f;
; #pragma unroll
;       for (int j = 0; j < 8; ++j) ss += v[j] * v[j];
;       ss = wave_sum(ss); const float rstd = rsqrtf(ss * (1.f / QRANK) + EPS);
;       const f32x4 w0 = *(const f32x4*)(p.q_norm + lane * 8), w1 = *(const f32x4*)(p.q_norm + lane * 8 + 4);
;       u32x4 o; o.x = cvt_pk_bf16(v[0] * rstd * w0[0], v[1] * rstd * w0[1]); o.y = cvt_pk_bf16(v[2] * rstd * w0[2], v[3] * rstd * w0[3]);
;       o.z = cvt_pk_bf16(v[4] * rstd * w1[0], v[5] * rstd * w1[1]); o.w = cvt_pk_bf16(v[6] * rstd * w1[2], v[7] * rstd * w1[3]);
;       *(u32x4*)(p.cqn + (long)lr * QRANK + lane * 8) = o;
;     }
;     {
;       const u32x2 raw = *(const u32x2*)(p.ckv + (long)row * KVRANK + lane * 4);
;       float v[4]; v[0] = bflo(raw.x); v[1] = bfhi(raw.x); v[2] = bflo(raw.y); v[3] = bfhi(raw.y);
;       float ss = v[0] * v[0] + v[1] * v[1] + v[2] * v[2] + v[3] * v[3];
;       ss = wave_sum(ss); const float rstd = rsqrtf(ss * (1.f / KVRANK) + EPS);
;       const f32x4 w0 = *(const f32x4*)(p.kv_norm + lane * 4);
;       u32x2 o; o.x = cvt_pk_bf16(v[0] * rstd * w0[0], v[1] * rstd * w0[1]); o.y = cvt_pk_bf16(v[2] * rstd * w0[2], v[3] * rstd * w0[3]);
;       *(u32x2*)(p.ckvn + (long)row * KVRANK + lane * 4) = o;
;     }
;     {
;       const float kv = p.kr[(long)row * ROPE + lane];
;       const float other = __shfl_xor(kv, 32);
;       float o = kv;
;       int b, key; row_to_bkey(row, b, key);
;       if (row >= NCTX) {
;         const int t = (row - NCTX) & 4095, a = lane & 31;
;         const float cs = p.rope[t * 64 + a], sn = p.rope[t * 64 + 32 + a];
;         o = lane < 32 ? kv * cs - other * sn : other * sn + kv * cs;
;       }
;       bf16_t* kd = p.kf + ((long)(b * NH) * KEYS + key) * QK + 128 + lane; const bf16_t ob = f2bf(o);
; #pragma unroll
;       for (int hh = 0; hh < NH; ++hh) kd[(long)hh * KEYS * QK] = ob;
.Lp3_kf3:
	v_mul_f32_e32 v128, v128, v135
	v_mul_f32_e32 v128, v128, v24
	v_mul_f32_e32 v129, v129, v135
	v_mul_f32_e32 v129, v129, v25
	v_mul_f32_e32 v130, v130, v135
	v_mul_f32_e32 v130, v130, v26
	v_mul_f32_e32 v131, v131, v135
	v_mul_f32_e32 v131, v131, v27
	v_cvt_pk_bf16_f32 v144, v128, v129
	v_cvt_pk_bf16_f32 v145, v130, v131
	s_lshl_b32 s31, s28, 9
	s_add_u32 s52, s10, s31
	s_addc_u32 s53, s11, 0
	global_store_dwordx2 v3, v[144:145], s[52:53]
	v_cvt_pk_bf16_f32 v146, v138, v138
	s_mul_i32 s54, s54, 0x8800
	s_add_u32 s54, s54, s55
	s_mul_i32 s54, s54, 0x180
	s_add_u32 s54, s54, 0x100
	s_add_u32 s52, s18, s54
	s_addc_u32 s53, s19, 0
	global_store_short v5, v146, s[52:53]
	s_add_u32 s52, s52, 0x198000
	s_addc_u32 s53, s53, 0
	global_store_short v5, v146, s[52:53]
	s_add_u32 s52, s52, 0x198000
	s_addc_u32 s53, s53, 0
	global_store_short v5, v146, s[52:53]
	s_add_u32 s52, s52, 0x198000
	s_addc_u32 s53, s53, 0
	global_store_short v5, v146, s[52:53]
	s_add_u32 s52, s52, 0x198000
	s_addc_u32 s53, s53, 0
	global_store_short v5, v146, s[52:53]
	s_add_u32 s52, s52, 0x198000
	s_addc_u32 s53, s53, 0
	global_store_short v5, v146, s[52:53]
	s_add_u32 s52, s52, 0x198000
	s_addc_u32 s53, s53, 0
	global_store_short v5, v146, s[52:53]
	s_add_u32 s52, s52, 0x198000
	s_addc_u32 s53, s53, 0
	global_store_short v5, v146, s[52:53]
	s_add_u32 s28, s28, s27
	s_cmp_lt_u32 s28, 0x4400
	s_cbranch_scc0 .Lp3_end
	s_waitcnt vmcnt(56)
	v_lshlrev_b32_e32 v120, 16, v68
	v_and_b32_e32 v121, 0xffff0000, v68
	v_lshlrev_b32_e32 v122, 16, v69
	v_and_b32_e32 v123, 0xffff0000, v69
	v_lshlrev_b32_e32 v124, 16, v70
	v_and_b32_e32 v125, 0xffff0000, v70
	v_lshlrev_b32_e32 v126, 16, v71
	v_and_b32_e32 v127, 0xffff0000, v71
	v_lshlrev_b32_e32 v128, 16, v72
	v_and_b32_e32 v129, 0xffff0000, v72
	v_lshlrev_b32_e32 v130, 16, v73
	v_and_b32_e32 v131, 0xffff0000, v73
	v_mul_f32_e32 v132, v120, v120
	v_fmac_f32_e32 v132, v121, v121
	v_fmac_f32_e32 v132, v122, v122
	v_fmac_f32_e32 v132, v123, v123
	v_fmac_f32_e32 v132, v124, v124
	v_fmac_f32_e32 v132, v125, v125
	v_fmac_f32_e32 v132, v126, v126
	v_fmac_f32_e32 v132, v127, v127
	v_mul_f32_e32 v133, v128, v128
	v_fmac_f32_e32 v133, v129, v129
	v_fmac_f32_e32 v133, v130, v130
	v_fmac_f32_e32 v133, v131, v131
	ds_bpermute_b32 v136, v8, v74
	ds_bpermute_b32 v134, v8, v132
	ds_bpermute_b32 v135, v8, v133
	s_waitcnt lgkmcnt(0)
	v_add_f32_e32 v132, v132, v134
	v_add_f32_e32 v133, v133, v135
	ds_bpermute_b32 v134, v9, v132
	ds_bpermute_b32 v135, v9, v133
	s_waitcnt lgkmcnt(0)
	v_add_f32_e32 v132, v132, v134
	v_add_f32_e32 v133, v133, v135
	ds_bpermute_b32 v134, v10, v132
	ds_bpermute_b32 v135, v10, v133
	s_waitcnt lgkmcnt(0)
	v_add_f32_e32 v132, v132, v134
	v_add_f32_e32 v133, v133, v135
	ds_bpermute_b32 v134, v11, v132
	ds_bpermute_b32 v135, v11, v133
	s_waitcnt lgkmcnt(0)
	v_add_f32_e32 v132, v132, v134
	v_add_f32_e32 v133, v133, v135
	ds_bpermute_b32 v134, v12, v132
	ds_bpermute_b32 v135, v12, v133
	s_waitcnt lgkmcnt(0)
	v_add_f32_e32 v132, v132, v134
	v_add_f32_e32 v133, v133, v135
	ds_bpermute_b32 v134, v13, v132
	ds_bpermute_b32 v135, v13, v133
	s_waitcnt lgkmcnt(0)
	v_add_f32_e32 v132, v132, v134
	v_add_f32_e32 v133, v133, v135
	v_mov_b32_e32 v134, 0x358637bd
	v_mov_b32_e32 v135, 0x358637bd
	v_fmac_f32_e32 v134, 0x3b000000, v132
	v_fmac_f32_e32 v135, 0x3b800000, v133
	v_rsq_f32_e32 v134, v134
	v_rsq_f32_e32 v135, v135
	s_sub_u32 s30, s28, 0x400
	s_cmp_lt_i32 s30, 0
	s_cbranch_scc1 .Lp3_ctx4
	v_mul_f32_e32 v120, v120, v134
	v_mul_f32_e32 v120, v120, v16
	v_mul_f32_e32 v121, v121, v134
	v_mul_f32_e32 v121, v121, v17
	v_mul_f32_e32 v122, v122, v134
	v_mul_f32_e32 v122, v122, v18
	v_mul_f32_e32 v123, v123, v134
	v_mul_f32_e32 v123, v123, v19
	v_mul_f32_e32 v124, v124, v134
	v_mul_f32_e32 v124, v124, v20
	v_mul_f32_e32 v125, v125, v134
	v_mul_f32_e32 v125, v125, v21
	v_mul_f32_e32 v126, v126, v134
	v_mul_f32_e32 v126, v126, v22
	v_mul_f32_e32 v127, v127, v134
	v_mul_f32_e32 v127, v127, v23
	v_cvt_pk_bf16_f32 v140, v120, v121
	v_cvt_pk_bf16_f32 v141, v122, v123
	v_cvt_pk_bf16_f32 v142, v124, v125
	v_cvt_pk_bf16_f32 v143, v126, v127
	s_lshl_b32 s31, s30, 10
	s_add_u32 s52, s6, s31
	s_addc_u32 s53, s7, 0
	global_store_dwordx4 v2, v[140:143], s[52:53]
	v_mul_f32_e32 v137, v136, v76
	v_fma_f32 v138, v74, v75, -v137
	v_fma_f32 v139, v74, v75, v137
	v_cndmask_b32_e64 v138, v139, v138, s[24:25]
	s_lshr_b32 s54, s30, 12
	s_and_b32 s55, s30, 0xfff
	s_add_u32 s55, s55, 0x100
	s_branch .Lp3_kf4
.Lp3_ctx4:
	v_mov_b32_e32 v138, v74
	s_lshr_b32 s54, s28, 8
	s_and_b32 s55, s28, 0xff
; DEV float bflo(unsigned v) { return __uint_as_float(v << 16); }
; DEV float bfhi(unsigned v) { return __uint_as_float(v & 0xffff0000u); }
; DEV void phase3_rows(CParams& p, int wg, int nwg) {
;     ...
;     if (row >= NCTX) {
;       const int lr = row - NCTX;
;       const u32x4 raw = *(const u32x4*)(p.cq + (long)lr * QRANK + lane * 8);
;       float v[8]; v[0] = bflo(raw.x); v[1] = bfhi(raw.x); v[2] = bflo(raw.y); v[3] = bfhi(raw.y); v[4] = bflo(raw.z); v[5] = bfhi(raw.z); v[6] = bflo(raw.w); v[7] = bfhi(raw.w);
;       float ss = 0.f;
; #pragma unroll
;       for (int j = 0; j < 8; ++j) ss += v[j] * v[j];
;       ss = wave_sum(ss); const float rstd = rsqrtf(ss * (1.f / QRANK) + EPS);
;       const f32x4 w0 = *(const f32x4*)(p.q_norm + lane * 8), w1 = *(const f32x4*)(p.q_norm + lane * 8 + 4);
;       u32x4 o; o.x = cvt_pk_bf16(v[0] * rstd * w0[0], v[1] * rstd * w0[1]); o.y = cvt_pk_bf16(v[2] * rstd * w0[2], v[3] * rstd * w0[3]);
;       o.z = cvt_pk_bf16(v[4] * rstd * w1[0], v[5] * rstd * w1[1]); o.w = cvt_pk_bf16(v[6] * rstd * w1[2], v[7] * rstd * w1[3]);
;       *(u32x4*)(p.cqn + (long)lr * QRANK + lane * 8) = o;
;     }
;     {
;       const u32x2 raw = *(const u32x2*)(p.ckv + (long)row * KVRANK + lane * 4);
;       float v[4]; v[0] = bflo(raw.x); v[1] = bfhi(raw.x); v[2] = bflo(raw.y); v[3] = bfhi(raw.y);
;       float ss = v[0] * v[0] + v[1] * v[1] + v[2] * v[2] + v[3] * v[3];
;       ss = wave_sum(ss); const float rstd = rsqrtf(ss * (1.f / KVRANK) + EPS);
;       const f32x4 w0 = *(const f32x4*)(p.kv_norm + lane * 4);
;       u32x2 o; o.x = cvt_pk_bf16(v[0] * rstd * w0[0], v[1] * rstd * w0[1]); o.y = cvt_pk_bf16(v[2] * rstd * w0[2], v[3] * rstd * w0[3]);
;       *(u32x2*)(p.ckvn + (long)row * KVRANK + lane * 4) = o;
;     }
;     {
;       const float kv = p.kr[(long)row * ROPE + lane];
;       const float other = __shfl_xor(kv, 32);
;       float o = kv;
;       int b, key; row_to_bkey(row, b, key);
;       if (row >= NCTX) {
;         const int t = (row - NCTX) & 4095, a = lane & 31;
;         const float cs = p.rope[t * 64 + a], sn = p.rope[t * 64 + 32 + a];
;         o = lane < 32 ? kv * cs - other * sn : other * sn + kv * cs;
;       }
;       bf16_t* kd = p.kf + ((long)(b * NH) * KEYS + key) * QK + 128 + lane; const bf16_t ob = f2bf(o);
; #pragma unroll
;       for (int hh = 0; hh < NH; ++hh) kd[(long)hh * KEYS * QK] = ob;
.Lp3_kf4:
	v_mul_f32_e32 v128, v128, v135
	v_mul_f32_e32 v128, v128, v24
	v_mul_f32_e32 v129, v129, v135
	v_mul_f32_e32 v129, v129, v25
	v_mul_f32_e32 v130, v130, v135
	v_mul_f32_e32 v130, v130, v26
	v_mul_f32_e32 v131, v131, v135
	v_mul_f32_e32 v131, v131, v27
	v_cvt_pk_bf16_f32 v144, v128, v129
	v_cvt_pk_bf16_f32 v145, v130, v131
	s_lshl_b32 s31, s28, 9
	s_add_u32 s52, s10, s31
	s_addc_u32 s53, s11, 0
	global_store_dwordx2 v3, v[144:145], s[52:53]
	v_cvt_pk_bf16_f32 v146, v138, v138
	s_mul_i32 s54, s54, 0x8800
	s_add_u32 s54, s54, s55
	s_mul_i32 s54, s54, 0x180
	s_add_u32 s54, s54, 0x100
	s_add_u32 s52, s18, s54
	s_addc_u32 s53, s19, 0
	global_store_short v5, v146, s[52:53]
	s_add_u32 s52, s52, 0x198000
	s_addc_u32 s53, s53, 0
	global_store_short v5, v146, s[52:53]
	s_add_u32 s52, s52, 0x198000
	s_addc_u32 s53, s53, 0
	global_store_short v5, v146, s[52:53]
	s_add_u32 s52, s52, 0x198000
	s_addc_u32 s53, s53, 0
	global_store_short v5, v146, s[52:53]
	s_add_u32 s52, s52, 0x198000
	s_addc_u32 s53, s53, 0
	global_store_short v5, v146, s[52:53]
	s_add_u32 s52, s52, 0x198000
	s_addc_u32 s53, s53, 0
	global_store_short v5, v146, s[52:53]
	s_add_u32 s52, s52, 0x198000
	s_addc_u32 s53, s53, 0
	global_store_short v5, v146, s[52:53]
	s_add_u32 s52, s52, 0x198000
	s_addc_u32 s53, s53, 0
	global_store_short v5, v146, s[52:53]
	s_add_u32 s28, s28, s27
	s_cmp_lt_u32 s28, 0x4400
	s_cbranch_scc0 .Lp3_end
	s_waitcnt vmcnt(60)
	v_lshlrev_b32_e32 v120, 16, v78
	v_and_b32_e32 v121, 0xffff0000, v78
	v_lshlrev_b32_e32 v122, 16, v79
	v_and_b32_e32 v123, 0xffff0000, v79
	v_lshlrev_b32_e32 v124, 16, v80
	v_and_b32_e32 v125, 0xffff0000, v80
	v_lshlrev_b32_e32 v126, 16, v81
	v_and_b32_e32 v127, 0xffff0000, v81
	v_lshlrev_b32_e32 v128, 16, v82
	v_and_b32_e32 v129, 0xffff0000, v82
	v_lshlrev_b32_e32 v130, 16, v83
	v_and_b32_e32 v131, 0xffff0000, v83
	v_mul_f32_e32 v132, v120, v120
	v_fmac_f32_e32 v132, v121, v121
	v_fmac_f32_e32 v132, v122, v122
	v_fmac_f32_e32 v132, v123, v123
	v_fmac_f32_e32 v132, v124, v124
	v_fmac_f32_e32 v132, v125, v125
	v_fmac_f32_e32 v132, v126, v126
	v_fmac_f32_e32 v132, v127, v127
	v_mul_f32_e32 v133, v128, v128
	v_fmac_f32_e32 v133, v129, v129
	v_fmac_f32_e32 v133, v130, v130
	v_fmac_f32_e32 v133, v131, v131
	ds_bpermute_b32 v136, v8, v84
	ds_bpermute_b32 v134, v8, v132
	ds_bpermute_b32 v135, v8, v133
	s_waitcnt lgkmcnt(0)
	v_add_f32_e32 v132, v132, v134
	v_add_f32_e32 v133, v133, v135
	ds_bpermute_b32 v134, v9, v132
	ds_bpermute_b32 v135, v9, v133
	s_waitcnt lgkmcnt(0)
	v_add_f32_e32 v132, v132, v134
	v_add_f32_e32 v133, v133, v135
	ds_bpermute_b32 v134, v10, v132
	ds_bpermute_b32 v135, v10, v133
	s_waitcnt lgkmcnt(0)
	v_add_f32_e32 v132, v132, v134
	v_add_f32_e32 v133, v133, v135
	ds_bpermute_b32 v134, v11, v132
	ds_bpermute_b32 v135, v11, v133
	s_waitcnt lgkmcnt(0)
	v_add_f32_e32 v132, v132, v134
	v_add_f32_e32 v133, v133, v135
	ds_bpermute_b32 v134, v12, v132
	ds_bpermute_b32 v135, v12, v133
	s_waitcnt lgkmcnt(0)
	v_add_f32_e32 v132, v132, v134
	v_add_f32_e32 v133, v133, v135
	ds_bpermute_b32 v134, v13, v132
	ds_bpermute_b32 v135, v13, v133
	s_waitcnt lgkmcnt(0)
	v_add_f32_e32 v132, v132, v134
	v_add_f32_e32 v133, v133, v135
	v_mov_b32_e32 v134, 0x358637bd
	v_mov_b32_e32 v135, 0x358637bd
	v_fmac_f32_e32 v134, 0x3b000000, v132
	v_fmac_f32_e32 v135, 0x3b800000, v133
	v_rsq_f32_e32 v134, v134
	v_rsq_f32_e32 v135, v135
	s_sub_u32 s30, s28, 0x400
	s_cmp_lt_i32 s30, 0
	s_cbranch_scc1 .Lp3_ctx5
	v_mul_f32_e32 v120, v120, v134
	v_mul_f32_e32 v120, v120, v16
	v_mul_f32_e32 v121, v121, v134
	v_mul_f32_e32 v121, v121, v17
	v_mul_f32_e32 v122, v122, v134
	v_mul_f32_e32 v122, v122, v18
	v_mul_f32_e32 v123, v123, v134
	v_mul_f32_e32 v123, v123, v19
	v_mul_f32_e32 v124, v124, v134
	v_mul_f32_e32 v124, v124, v20
	v_mul_f32_e32 v125, v125, v134
	v_mul_f32_e32 v125, v125, v21
	v_mul_f32_e32 v126, v126, v134
	v_mul_f32_e32 v126, v126, v22
	v_mul_f32_e32 v127, v127, v134
	v_mul_f32_e32 v127, v127, v23
	v_cvt_pk_bf16_f32 v140, v120, v121
	v_cvt_pk_bf16_f32 v141, v122, v123
	v_cvt_pk_bf16_f32 v142, v124, v125
	v_cvt_pk_bf16_f32 v143, v126, v127
	s_lshl_b32 s31, s30, 10
	s_add_u32 s52, s6, s31
	s_addc_u32 s53, s7, 0
	global_store_dwordx4 v2, v[140:143], s[52:53]
	v_mul_f32_e32 v137, v136, v86
	v_fma_f32 v138, v84, v85, -v137
	v_fma_f32 v139, v84, v85, v137
	v_cndmask_b32_e64 v138, v139, v138, s[24:25]
	s_lshr_b32 s54, s30, 12
	s_and_b32 s55, s30, 0xfff
	s_add_u32 s55, s55, 0x100
	s_branch .Lp3_kf5
.Lp3_ctx5:
	v_mov_b32_e32 v138, v84
	s_lshr_b32 s54, s28, 8
	s_and_b32 s55, s28, 0xff
; DEV float bflo(unsigned v) { return __uint_as_float(v << 16); }
; DEV float bfhi(unsigned v) { return __uint_as_float(v & 0xffff0000u); }
; DEV void phase3_rows(CParams& p, int wg, int nwg) {
;     ...
;     if (row >= NCTX) {
;       const int lr = row - NCTX;
;       const u32x4 raw = *(const u32x4*)(p.cq + (long)lr * QRANK + lane * 8);
;       float v[8]; v[0] = bflo(raw.x); v[1] = bfhi(raw.x); v[2] = bflo(raw.y); v[3] = bfhi(raw.y); v[4] = bflo(raw.z); v[5] = bfhi(raw.z); v[6] = bflo(raw.w); v[7] = bfhi(raw.w);
;       float ss = 0.f;
; #pragma unroll
;       for (int j = 0; j < 8; ++j) ss += v[j] * v[j];
;       ss = wave_sum(ss); const float rstd = rsqrtf(ss * (1.f / QRANK) + EPS);
;       const f32x4 w0 = *(const f32x4*)(p.q_norm + lane * 8), w1 = *(const f32x4*)(p.q_norm + lane * 8 + 4);
;       u32x4 o; o.x = cvt_pk_bf16(v[0] * rstd * w0[0], v[1] * rstd * w0[1]); o.y = cvt_pk_bf16(v[2] * rstd * w0[2], v[3] * rstd * w0[3]);
;       o.z = cvt_pk_bf16(v[4] * rstd * w1[0], v[5] * rstd * w1[1]); o.w = cvt_pk_bf16(v[6] * rstd * w1[2], v[7] * rstd * w1[3]);
;       *(u32x4*)(p.cqn + (long)lr * QRANK + lane * 8) = o;
;     }
;     {
;       const u32x2 raw = *(const u32x2*)(p.ckv + (long)row * KVRANK + lane * 4);
;       float v[4]; v[0] = bflo(raw.x); v[1] = bfhi(raw.x); v[2] = bflo(raw.y); v[3] = bfhi(raw.y);
;       float ss = v[0] * v[0] + v[1] * v[1] + v[2] * v[2] + v[3] * v[3];
;       ss = wave_sum(ss); const float rstd = rsqrtf(ss * (1.f / KVRANK) + EPS);
;       const f32x4 w0 = *(const f32x4*)(p.kv_norm + lane * 4);
;       u32x2 o; o.x = cvt_pk_bf16(v[0] * rstd * w0[0], v[1] * rstd * w0[1]); o.y = cvt_pk_bf16(v[2] * rstd * w0[2], v[3] * rstd * w0[3]);
;       *(u32x2*)(p.ckvn + (long)row * KVRANK + lane * 4) = o;
;     }
;     {
;       const float kv = p.kr[(long)row * ROPE + lane];
;       const float other = __shfl_xor(kv, 32);
;       float o = kv;
;       int b, key; row_to_bkey(row, b, key);
;       if (row >= NCTX) {
;         const int t = (row - NCTX) & 4095, a = lane & 31;
;         const float cs = p.rope[t * 64 + a], sn = p.rope[t * 64 + 32 + a];
;         o = lane < 32 ? kv * cs - other * sn : other * sn + kv * cs;
;       }
;       bf16_t* kd = p.kf + ((long)(b * NH) * KEYS + key) * QK + 128 + lane; const bf16_t ob = f2bf(o);
; #pragma unroll
;       for (int hh = 0; hh < NH; ++hh) kd[(long)hh * KEYS * QK] = ob;
.Lp3_kf5:
	v_mul_f32_e32 v128, v128, v135
	v_mul_f32_e32 v128, v128, v24
	v_mul_f32_e32 v129, v129, v135
	v_mul_f32_e32 v129, v129, v25
	v_mul_f32_e32 v130, v130, v135
	v_mul_f32_e32 v130, v130, v26
	v_mul_f32_e32 v131, v131, v135
	v_mul_f32_e32 v131, v131, v27
	v_cvt_pk_bf16_f32 v144, v128, v129
	v_cvt_pk_bf16_f32 v145, v130, v131
	s_lshl_b32 s31, s28, 9
	s_add_u32 s52, s10, s31
	s_addc_u32 s53, s11, 0
	global_store_dwordx2 v3, v[144:145], s[52:53]
	v_cvt_pk_bf16_f32 v146, v138, v138
	s_mul_i32 s54, s54, 0x8800
	s_add_u32 s54, s54, s55
	s_mul_i32 s54, s54, 0x180
	s_add_u32 s54, s54, 0x100
	s_add_u32 s52, s18, s54
	s_addc_u32 s53, s19, 0
	global_store_short v5, v146, s[52:53]
	s_add_u32 s52, s52, 0x198000
	s_addc_u32 s53, s53, 0
	global_store_short v5, v146, s[52:53]
	s_add_u32 s52, s52, 0x198000
	s_addc_u32 s53, s53, 0
	global_store_short v5, v146, s[52:53]
	s_add_u32 s52, s52, 0x198000
	s_addc_u32 s53, s53, 0
	global_store_short v5, v146, s[52:53]
	s_add_u32 s52, s52, 0x198000
	s_addc_u32 s53, s53, 0
	global_store_short v5, v146, s[52:53]
	s_add_u32 s52, s52, 0x198000
	s_addc_u32 s53, s53, 0
	global_store_short v5, v146, s[52:53]
	s_add_u32 s52, s52, 0x198000
	s_addc_u32 s53, s53, 0
	global_store_short v5, v146, s[52:53]
	s_add_u32 s52, s52, 0x198000
	s_addc_u32 s53, s53, 0
	global_store_short v5, v146, s[52:53]
	s_add_u32 s28, s28, s27
	s_cmp_lt_u32 s28, 0x4400
	s_cbranch_scc0 .Lp3_end
	s_waitcnt vmcnt(63)
	v_lshlrev_b32_e32 v120, 16, v88
	v_and_b32_e32 v121, 0xffff0000, v88
	v_lshlrev_b32_e32 v122, 16, v89
	v_and_b32_e32 v123, 0xffff0000, v89
	v_lshlrev_b32_e32 v124, 16, v90
	v_and_b32_e32 v125, 0xffff0000, v90
	v_lshlrev_b32_e32 v126, 16, v91
	v_and_b32_e32 v127, 0xffff0000, v91
	v_lshlrev_b32_e32 v128, 16, v92
	v_and_b32_e32 v129, 0xffff0000, v92
	v_lshlrev_b32_e32 v130, 16, v93
	v_and_b32_e32 v131, 0xffff0000, v93
	v_mul_f32_e32 v132, v120, v120
	v_fmac_f32_e32 v132, v121, v121
	v_fmac_f32_e32 v132, v122, v122
	v_fmac_f32_e32 v132, v123, v123
	v_fmac_f32_e32 v132, v124, v124
	v_fmac_f32_e32 v132, v125, v125
	v_fmac_f32_e32 v132, v126, v126
	v_fmac_f32_e32 v132, v127, v127
	v_mul_f32_e32 v133, v128, v128
	v_fmac_f32_e32 v133, v129, v129
	v_fmac_f32_e32 v133, v130, v130
	v_fmac_f32_e32 v133, v131, v131
	ds_bpermute_b32 v136, v8, v94
	ds_bpermute_b32 v134, v8, v132
	ds_bpermute_b32 v135, v8, v133
	s_waitcnt lgkmcnt(0)
	v_add_f32_e32 v132, v132, v134
	v_add_f32_e32 v133, v133, v135
	ds_bpermute_b32 v134, v9, v132
	ds_bpermute_b32 v135, v9, v133
	s_waitcnt lgkmcnt(0)
	v_add_f32_e32 v132, v132, v134
	v_add_f32_e32 v133, v133, v135
	ds_bpermute_b32 v134, v10, v132
	ds_bpermute_b32 v135, v10, v133
	s_waitcnt lgkmcnt(0)
	v_add_f32_e32 v132, v132, v134
	v_add_f32_e32 v133, v133, v135
	ds_bpermute_b32 v134, v11, v132
	ds_bpermute_b32 v135, v11, v133
	s_waitcnt lgkmcnt(0)
	v_add_f32_e32 v132, v132, v134
	v_add_f32_e32 v133, v133, v135
	ds_bpermute_b32 v134, v12, v132
	ds_bpermute_b32 v135, v12, v133
	s_waitcnt lgkmcnt(0)
	v_add_f32_e32 v132, v132, v134
	v_add_f32_e32 v133, v133, v135
	ds_bpermute_b32 v134, v13, v132
	ds_bpermute_b32 v135, v13, v133
	s_waitcnt lgkmcnt(0)
	v_add_f32_e32 v132, v132, v134
	v_add_f32_e32 v133, v133, v135
	v_mov_b32_e32 v134, 0x358637bd
	v_mov_b32_e32 v135, 0x358637bd
	v_fmac_f32_e32 v134, 0x3b000000, v132
	v_fmac_f32_e32 v135, 0x3b800000, v133
	v_rsq_f32_e32 v134, v134
	v_rsq_f32_e32 v135, v135
	s_sub_u32 s30, s28, 0x400
	s_cmp_lt_i32 s30, 0
	s_cbranch_scc1 .Lp3_ctx6
	v_mul_f32_e32 v120, v120, v134
	v_mul_f32_e32 v120, v120, v16
	v_mul_f32_e32 v121, v121, v134
	v_mul_f32_e32 v121, v121, v17
	v_mul_f32_e32 v122, v122, v134
	v_mul_f32_e32 v122, v122, v18
	v_mul_f32_e32 v123, v123, v134
	v_mul_f32_e32 v123, v123, v19
	v_mul_f32_e32 v124, v124, v134
	v_mul_f32_e32 v124, v124, v20
	v_mul_f32_e32 v125, v125, v134
	v_mul_f32_e32 v125, v125, v21
	v_mul_f32_e32 v126, v126, v134
	v_mul_f32_e32 v126, v126, v22
	v_mul_f32_e32 v127, v127, v134
	v_mul_f32_e32 v127, v127, v23
	v_cvt_pk_bf16_f32 v140, v120, v121
	v_cvt_pk_bf16_f32 v141, v122, v123
	v_cvt_pk_bf16_f32 v142, v124, v125
	v_cvt_pk_bf16_f32 v143, v126, v127
	s_lshl_b32 s31, s30, 10
	s_add_u32 s52, s6, s31
	s_addc_u32 s53, s7, 0
	global_store_dwordx4 v2, v[140:143], s[52:53]
	v_mul_f32_e32 v137, v136, v96
	v_fma_f32 v138, v94, v95, -v137
	v_fma_f32 v139, v94, v95, v137
	v_cndmask_b32_e64 v138, v139, v138, s[24:25]
	s_lshr_b32 s54, s30, 12
	s_and_b32 s55, s30, 0xfff
	s_add_u32 s55, s55, 0x100
	s_branch .Lp3_kf6
.Lp3_ctx6:
	v_mov_b32_e32 v138, v94
	s_lshr_b32 s54, s28, 8
	s_and_b32 s55, s28, 0xff
; DEV float bflo(unsigned v) { return __uint_as_float(v << 16); }
; DEV float bfhi(unsigned v) { return __uint_as_float(v & 0xffff0000u); }
; DEV void phase3_rows(CParams& p, int wg, int nwg) {
;     ...
;     if (row >= NCTX) {
;       const int lr = row - NCTX;
;       const u32x4 raw = *(const u32x4*)(p.cq + (long)lr * QRANK + lane * 8);
;       float v[8]; v[0] = bflo(raw.x); v[1] = bfhi(raw.x); v[2] = bflo(raw.y); v[3] = bfhi(raw.y); v[4] = bflo(raw.z); v[5] = bfhi(raw.z); v[6] = bflo(raw.w); v[7] = bfhi(raw.w);
;       float ss = 0.f;
; #pragma unroll
;       for (int j = 0; j < 8; ++j) ss += v[j] * v[j];
;       ss = wave_sum(ss); const float rstd = rsqrtf(ss * (1.f / QRANK) + EPS);
;       const f32x4 w0 = *(const f32x4*)(p.q_norm + lane * 8), w1 = *(const f32x4*)(p.q_norm + lane * 8 + 4);
;       u32x4 o; o.x = cvt_pk_bf16(v[0] * rstd * w0[0], v[1] * rstd * w0[1]); o.y = cvt_pk_bf16(v[2] * rstd * w0[2], v[3] * rstd * w0[3]);
;       o.z = cvt_pk_bf16(v[4] * rstd * w1[0], v[5] * rstd * w1[1]); o.w = cvt_pk_bf16(v[6] * rstd * w1[2], v[7] * rstd * w1[3]);
;       *(u32x4*)(p.cqn + (long)lr * QRANK + lane * 8) = o;
;     }
;     {
;       const u32x2 raw = *(const u32x2*)(p.ckv + (long)row * KVRANK + lane * 4);
;       float v[4]; v[0] = bflo(raw.x); v[1] = bfhi(raw.x); v[2] = bflo(raw.y); v[3] = bfhi(raw.y);
;       float ss = v[0] * v[0] + v[1] * v[1] + v[2] * v[2] + v[3] * v[3];
;       ss = wave_sum(ss); const float rstd = rsqrtf(ss * (1.f / KVRANK) + EPS);
;       const f32x4 w0 = *(const f32x4*)(p.kv_norm + lane * 4);
;       u32x2 o; o.x = cvt_pk_bf16(v[0] * rstd * w0[0], v[1] * rstd * w0[1]); o.y = cvt_pk_bf16(v[2] * rstd * w0[2], v[3] * rstd * w0[3]);
;       *(u32x2*)(p.ckvn + (long)row * KVRANK + lane * 4) = o;
;     }
;     {
;       const float kv = p.kr[(long)row * ROPE + lane];
;       const float other = __shfl_xor(kv, 32);
;       float o = kv;
;       int b, key; row_to_bkey(row, b, key);
;       if (row >= NCTX) {
;         const int t = (row - NCTX) & 4095, a = lane & 31;
;         const float cs = p.rope[t * 64 + a], sn = p.rope[t * 64 + 32 + a];
;         o = lane < 32 ? kv * cs - other * sn : other * sn + kv * cs;
;       }
;       bf16_t* kd = p.kf + ((long)(b * NH) * KEYS + key) * QK + 128 + lane; const bf16_t ob = f2bf(o);
; #pragma unroll
;       for (int hh = 0; hh < NH; ++hh) kd[(long)hh * KEYS * QK] = ob;
.Lp3_kf6:
	v_mul_f32_e32 v128, v128, v135
	v_mul_f32_e32 v128, v128, v24
	v_mul_f32_e32 v129, v129, v135
	v_mul_f32_e32 v129, v129, v25
	v_mul_f32_e32 v130, v130, v135
	v_mul_f32_e32 v130, v130, v26
	v_mul_f32_e32 v131, v131, v135
	v_mul_f32_e32 v131, v131, v27
	v_cvt_pk_bf16_f32 v144, v128, v129
	v_cvt_pk_bf16_f32 v145, v130, v131
	s_lshl_b32 s31, s28, 9
	s_add_u32 s52, s10, s31
	s_addc_u32 s53, s11, 0
	global_store_dwordx2 v3, v[144:145], s[52:53]
	v_cvt_pk_bf16_f32 v146, v138, v138
	s_mul_i32 s54, s54, 0x8800
	s_add_u32 s54, s54, s55
	s_mul_i32 s54, s54, 0x180
	s_add_u32 s54, s54, 0x100
	s_add_u32 s52, s18, s54
	s_addc_u32 s53, s19, 0
	global_store_short v5, v146, s[52:53]
	s_add_u32 s52, s52, 0x198000
	s_addc_u32 s53, s53, 0
	global_store_short v5, v146, s[52:53]
	s_add_u32 s52, s52, 0x198000
	s_addc_u32 s53, s53, 0
	global_store_short v5, v146, s[52:53]
	s_add_u32 s52, s52, 0x198000
	s_addc_u32 s53, s53, 0
	global_store_short v5, v146, s[52:53]
	s_add_u32 s52, s52, 0x198000
	s_addc_u32 s53, s53, 0
	global_store_short v5, v146, s[52:53]
	s_add_u32 s52, s52, 0x198000
	s_addc_u32 s53, s53, 0
	global_store_short v5, v146, s[52:53]
	s_add_u32 s52, s52, 0x198000
	s_addc_u32 s53, s53, 0
	global_store_short v5, v146, s[52:53]
	s_add_u32 s52, s52, 0x198000
	s_addc_u32 s53, s53, 0
	global_store_short v5, v146, s[52:53]
	s_add_u32 s28, s28, s27
	s_cmp_lt_u32 s28, 0x4400
	s_cbranch_scc0 .Lp3_end
	s_waitcnt vmcnt(63)
	v_lshlrev_b32_e32 v120, 16, v98
	v_and_b32_e32 v121, 0xffff0000, v98
	v_lshlrev_b32_e32 v122, 16, v99
	v_and_b32_e32 v123, 0xffff0000, v99
	v_lshlrev_b32_e32 v124, 16, v100
	v_and_b32_e32 v125, 0xffff0000, v100
	v_lshlrev_b32_e32 v126, 16, v101
	v_and_b32_e32 v127, 0xffff0000, v101
	v_lshlrev_b32_e32 v128, 16, v102
	v_and_b32_e32 v129, 0xffff0000, v102
	v_lshlrev_b32_e32 v130, 16, v103
	v_and_b32_e32 v131, 0xffff0000, v103
	v_mul_f32_e32 v132, v120, v120
	v_fmac_f32_e32 v132, v121, v121
	v_fmac_f32_e32 v132, v122, v122
	v_fmac_f32_e32 v132, v123, v123
	v_fmac_f32_e32 v132, v124, v124
	v_fmac_f32_e32 v132, v125, v125
	v_fmac_f32_e32 v132, v126, v126
	v_fmac_f32_e32 v132, v127, v127
	v_mul_f32_e32 v133, v128, v128
	v_fmac_f32_e32 v133, v129, v129
	v_fmac_f32_e32 v133, v130, v130
	v_fmac_f32_e32 v133, v131, v131
	ds_bpermute_b32 v136, v8, v104
	ds_bpermute_b32 v134, v8, v132
	ds_bpermute_b32 v135, v8, v133
	s_waitcnt lgkmcnt(0)
	v_add_f32_e32 v132, v132, v134
	v_add_f32_e32 v133, v133, v135
	ds_bpermute_b32 v134, v9, v132
	ds_bpermute_b32 v135, v9, v133
	s_waitcnt lgkmcnt(0)
	v_add_f32_e32 v132, v132, v134
	v_add_f32_e32 v133, v133, v135
	ds_bpermute_b32 v134, v10, v132
	ds_bpermute_b32 v135, v10, v133
	s_waitcnt lgkmcnt(0)
	v_add_f32_e32 v132, v132, v134
	v_add_f32_e32 v133, v133, v135
	ds_bpermute_b32 v134, v11, v132
	ds_bpermute_b32 v135, v11, v133
	s_waitcnt lgkmcnt(0)
	v_add_f32_e32 v132, v132, v134
	v_add_f32_e32 v133, v133, v135
	ds_bpermute_b32 v134, v12, v132
	ds_bpermute_b32 v135, v12, v133
	s_waitcnt lgkmcnt(0)
	v_add_f32_e32 v132, v132, v134
	v_add_f32_e32 v133, v133, v135
	ds_bpermute_b32 v134, v13, v132
	ds_bpermute_b32 v135, v13, v133
	s_waitcnt lgkmcnt(0)
	v_add_f32_e32 v132, v132, v134
	v_add_f32_e32 v133, v133, v135
	v_mov_b32_e32 v134, 0x358637bd
	v_mov_b32_e32 v135, 0x358637bd
	v_fmac_f32_e32 v134, 0x3b000000, v132
	v_fmac_f32_e32 v135, 0x3b800000, v133
	v_rsq_f32_e32 v134, v134
	v_rsq_f32_e32 v135, v135
	s_sub_u32 s30, s28, 0x400
	s_cmp_lt_i32 s30, 0
	s_cbranch_scc1 .Lp3_ctx7
	v_mul_f32_e32 v120, v120, v134
	v_mul_f32_e32 v120, v120, v16
	v_mul_f32_e32 v121, v121, v134
	v_mul_f32_e32 v121, v121, v17
	v_mul_f32_e32 v122, v122, v134
	v_mul_f32_e32 v122, v122, v18
	v_mul_f32_e32 v123, v123, v134
	v_mul_f32_e32 v123, v123, v19
	v_mul_f32_e32 v124, v124, v134
	v_mul_f32_e32 v124, v124, v20
	v_mul_f32_e32 v125, v125, v134
	v_mul_f32_e32 v125, v125, v21
	v_mul_f32_e32 v126, v126, v134
	v_mul_f32_e32 v126, v126, v22
	v_mul_f32_e32 v127, v127, v134
	v_mul_f32_e32 v127, v127, v23
	v_cvt_pk_bf16_f32 v140, v120, v121
	v_cvt_pk_bf16_f32 v141, v122, v123
	v_cvt_pk_bf16_f32 v142, v124, v125
	v_cvt_pk_bf16_f32 v143, v126, v127
	s_lshl_b32 s31, s30, 10
	s_add_u32 s52, s6, s31
	s_addc_u32 s53, s7, 0
	global_store_dwordx4 v2, v[140:143], s[52:53]
	v_mul_f32_e32 v137, v136, v106
	v_fma_f32 v138, v104, v105, -v137
	v_fma_f32 v139, v104, v105, v137
	v_cndmask_b32_e64 v138, v139, v138, s[24:25]
	s_lshr_b32 s54, s30, 12
	s_and_b32 s55, s30, 0xfff
	s_add_u32 s55, s55, 0x100
	s_branch .Lp3_kf7
.Lp3_ctx7:
	v_mov_b32_e32 v138, v104
	s_lshr_b32 s54, s28, 8
	s_and_b32 s55, s28, 0xff
; DEV unsigned cvt_pk_bf16(float lo, float hi) { const f32x2 v = {lo, hi}; const bf16n2 r = __builtin_convertvector(v, bf16n2); return __builtin_bit_cast(unsigned, r); }
; DEV float bflo(unsigned v) { return __uint_as_float(v << 16); }
; DEV float bfhi(unsigned v) { return __uint_as_float(v & 0xffff0000u); }
; DEV void row_to_bkey(int row, int& b, int& key) { if (row < NCTX) { b = row >> 8; key = row & 255; } else { const int r = row - NCTX; b = r >> 12; key = CTX + (r & 4095); } }
; DEV void phase3_rows(CParams& p, int wg, int nwg) {
;     ...
;       const u32x2 raw = *(const u32x2*)(p.ckv + (long)row * KVRANK + lane * 4);
;       float v[4]; v[0] = bflo(raw.x); v[1] = bfhi(raw.x); v[2] = bflo(raw.y); v[3] = bfhi(raw.y);
;       float ss = v[0] * v[0] + v[1] * v[1] + v[2] * v[2] + v[3] * v[3];
;       ss = wave_sum(ss); const float rstd = rsqrtf(ss * (1.f / KVRANK) + EPS);
;       const f32x4 w0 = *(const f32x4*)(p.kv_norm + lane * 4);
;       u32x2 o; o.x = cvt_pk_bf16(v[0] * rstd * w0[0], v[1] * rstd * w0[1]); o.y = cvt_pk_bf16(v[2] * rstd * w0[2], v[3] * rstd * w0[3]);
;       *(u32x2*)(p.ckvn + (long)row * KVRANK + lane * 4) = o;
;     }
;     {
;       const float kv = p.kr[(long)row * ROPE + lane];
;       const float other = __shfl_xor(kv, 32);
;       float o = kv;
;       int b, key; row_to_bkey(row, b, key);
;       if (row >= NCTX) {
;         const int t = (row - NCTX) & 4095, a = lane & 31;
;         const float cs = p.rope[t * 64 + a], sn = p.rope[t * 64 + 32 + a];
;         o = lane < 32 ? kv * cs - other * sn : other * sn + kv * cs;
;       }
;       bf16_t* kd = p.kf + ((long)(b * NH) * KEYS + key) * QK + 128 + lane; const bf16_t ob = f2bf(o);
; #pragma unroll
;       for (int hh = 0; hh < NH; ++hh) kd[(long)hh * KEYS * QK] = ob;
;     }
;   }
; __device__ __forceinline__ void xcd_barrier(const XcdBarrier& b) {
;     asm volatile("s_waitcnt vmcnt(0)" ::: "memory");
;     __syncthreads();
;     if (threadIdx.x == 0) {
;         unsigned* bar = b.bar;
;         __builtin_amdgcn_s_waitcnt(0);
;         unsigned nloc = b.st[0], nx = b.st[1];
;         if (nloc == 0u) { xcd_barrier_complete(bar, b.x, nloc, nx); b.st[0] = nloc; b.st[1] = nx; }
;         const unsigned old = xb_add(&bar[XB_XSUB(b.x)], 1u);
;         const unsigned gen = old / nloc;
.Lp3_kf7:
	v_mul_f32_e32 v128, v128, v135
	v_mul_f32_e32 v128, v128, v24
	v_mul_f32_e32 v129, v129, v135
	v_mul_f32_e32 v129, v129, v25
	v_mul_f32_e32 v130, v130, v135
	v_mul_f32_e32 v130, v130, v26
	v_mul_f32_e32 v131, v131, v135
	v_mul_f32_e32 v131, v131, v27
	v_cvt_pk_bf16_f32 v144, v128, v129
	v_cvt_pk_bf16_f32 v145, v130, v131
	s_lshl_b32 s31, s28, 9
	s_add_u32 s52, s10, s31
	s_addc_u32 s53, s11, 0
	global_store_dwordx2 v3, v[144:145], s[52:53]
	v_cvt_pk_bf16_f32 v146, v138, v138
	s_mul_i32 s54, s54, 0x8800
	s_add_u32 s54, s54, s55
	s_mul_i32 s54, s54, 0x180
	s_add_u32 s54, s54, 0x100
	s_add_u32 s52, s18, s54
	s_addc_u32 s53, s19, 0
	global_store_short v5, v146, s[52:53]
	s_add_u32 s52, s52, 0x198000
	s_addc_u32 s53, s53, 0
	global_store_short v5, v146, s[52:53]
	s_add_u32 s52, s52, 0x198000
	s_addc_u32 s53, s53, 0
	global_store_short v5, v146, s[52:53]
	s_add_u32 s52, s52, 0x198000
	s_addc_u32 s53, s53, 0
	global_store_short v5, v146, s[52:53]
	s_add_u32 s52, s52, 0x198000
	s_addc_u32 s53, s53, 0
	global_store_short v5, v146, s[52:53]
	s_add_u32 s52, s52, 0x198000
	s_addc_u32 s53, s53, 0
	global_store_short v5, v146, s[52:53]
	s_add_u32 s52, s52, 0x198000
	s_addc_u32 s53, s53, 0
	global_store_short v5, v146, s[52:53]
	s_add_u32 s52, s52, 0x198000
	s_addc_u32 s53, s53, 0
	global_store_short v5, v146, s[52:53]
	s_add_u32 s28, s28, s27
	s_cmp_lt_u32 s28, 0x4400
	s_cbranch_scc0 .Lp3_end
	s_waitcnt vmcnt(63)
	v_lshlrev_b32_e32 v120, 16, v108
	v_and_b32_e32 v121, 0xffff0000, v108
	v_lshlrev_b32_e32 v122, 16, v109
	v_and_b32_e32 v123, 0xffff0000, v109
	v_lshlrev_b32_e32 v124, 16, v110
	v_and_b32_e32 v125, 0xffff0000, v110
	v_lshlrev_b32_e32 v126, 16, v111
	v_and_b32_e32 v127, 0xffff0000, v111
	v_lshlrev_b32_e32 v128, 16, v112
	v_and_b32_e32 v129, 0xffff0000, v112
	v_lshlrev_b32_e32 v130, 16, v113
	v_and_b32_e32 v131, 0xffff0000, v113
	v_mul_f32_e32 v132, v120, v120
	v_fmac_f32_e32 v132, v121, v121
	v_fmac_f32_e32 v132, v122, v122
	v_fmac_f32_e32 v132, v123, v123
	v_fmac_f32_e32 v132, v124, v124
	v_fmac_f32_e32 v132, v125, v125
	v_fmac_f32_e32 v132, v126, v126
	v_fmac_f32_e32 v132, v127, v127
	v_mul_f32_e32 v133, v128, v128
	v_fmac_f32_e32 v133, v129, v129
	v_fmac_f32_e32 v133, v130, v130
	v_fmac_f32_e32 v133, v131, v131
	ds_bpermute_b32 v136, v8, v114
	ds_bpermute_b32 v134, v8, v132
	ds_bpermute_b32 v135, v8, v133
	s_waitcnt lgkmcnt(0)
	v_add_f32_e32 v132, v132, v134
	v_add_f32_e32 v133, v133, v135
	ds_bpermute_b32 v134, v9, v132
	ds_bpermute_b32 v135, v9, v133
	s_waitcnt lgkmcnt(0)
	v_add_f32_e32 v132, v132, v134
	v_add_f32_e32 v133, v133, v135
	ds_bpermute_b32 v134, v10, v132
	ds_bpermute_b32 v135, v10, v133
	s_waitcnt lgkmcnt(0)
	v_add_f32_e32 v132, v132, v134
	v_add_f32_e32 v133, v133, v135
	ds_bpermute_b32 v134, v11, v132
	ds_bpermute_b32 v135, v11, v133
	s_waitcnt lgkmcnt(0)
	v_add_f32_e32 v132, v132, v134
	v_add_f32_e32 v133, v133, v135
	ds_bpermute_b32 v134, v12, v132
	ds_bpermute_b32 v135, v12, v133
	s_waitcnt lgkmcnt(0)
	v_add_f32_e32 v132, v132, v134
	v_add_f32_e32 v133, v133, v135
	ds_bpermute_b32 v134, v13, v132
	ds_bpermute_b32 v135, v13, v133
	s_waitcnt lgkmcnt(0)
	v_add_f32_e32 v132, v132, v134
	v_add_f32_e32 v133, v133, v135
	v_mov_b32_e32 v134, 0x358637bd
	v_mov_b32_e32 v135, 0x358637bd
	v_fmac_f32_e32 v134, 0x3b000000, v132
	v_fmac_f32_e32 v135, 0x3b800000, v133
	v_rsq_f32_e32 v134, v134
	v_rsq_f32_e32 v135, v135
	s_sub_u32 s30, s28, 0x400
	s_cmp_lt_i32 s30, 0
	s_cbranch_scc1 .Lp3_ctx8
	v_mul_f32_e32 v120, v120, v134
	v_mul_f32_e32 v120, v120, v16
	v_mul_f32_e32 v121, v121, v134
	v_mul_f32_e32 v121, v121, v17
	v_mul_f32_e32 v122, v122, v134
	v_mul_f32_e32 v122, v122, v18
	v_mul_f32_e32 v123, v123, v134
	v_mul_f32_e32 v123, v123, v19
	v_mul_f32_e32 v124, v124, v134
	v_mul_f32_e32 v124, v124, v20
	v_mul_f32_e32 v125, v125, v134
	v_mul_f32_e32 v125, v125, v21
	v_mul_f32_e32 v126, v126, v134
	v_mul_f32_e32 v126, v126, v22
	v_mul_f32_e32 v127, v127, v134
	v_mul_f32_e32 v127, v127, v23
	v_cvt_pk_bf16_f32 v140, v120, v121
	v_cvt_pk_bf16_f32 v141, v122, v123
	v_cvt_pk_bf16_f32 v142, v124, v125
	v_cvt_pk_bf16_f32 v143, v126, v127
	s_lshl_b32 s31, s30, 10
	s_add_u32 s52, s6, s31
	s_addc_u32 s53, s7, 0
	global_store_dwordx4 v2, v[140:143], s[52:53]
	v_mul_f32_e32 v137, v136, v116
	v_fma_f32 v138, v114, v115, -v137
	v_fma_f32 v139, v114, v115, v137
	v_cndmask_b32_e64 v138, v139, v138, s[24:25]
	s_lshr_b32 s54, s30, 12
	s_and_b32 s55, s30, 0xfff
	s_add_u32 s55, s55, 0x100
	s_branch .Lp3_kf8
.Lp3_ctx8:
	v_mov_b32_e32 v138, v114
	s_lshr_b32 s54, s28, 8
	s_and_b32 s55, s28, 0xff
.Lp3_kf8:
	v_mul_f32_e32 v128, v128, v135
	v_mul_f32_e32 v128, v128, v24
	v_mul_f32_e32 v129, v129, v135
	v_mul_f32_e32 v129, v129, v25
	v_mul_f32_e32 v130, v130, v135
	v_mul_f32_e32 v130, v130, v26
	v_mul_f32_e32 v131, v131, v135
	v_mul_f32_e32 v131, v131, v27
	v_cvt_pk_bf16_f32 v144, v128, v129
	v_cvt_pk_bf16_f32 v145, v130, v131
	s_lshl_b32 s31, s28, 9
	s_add_u32 s52, s10, s31
	s_addc_u32 s53, s11, 0
	global_store_dwordx2 v3, v[144:145], s[52:53]
	v_cvt_pk_bf16_f32 v146, v138, v138
	s_mul_i32 s54, s54, 0x8800
	s_add_u32 s54, s54, s55
	s_mul_i32 s54, s54, 0x180
	s_add_u32 s54, s54, 0x100
	s_add_u32 s52, s18, s54
	s_addc_u32 s53, s19, 0
	global_store_short v5, v146, s[52:53]
	s_add_u32 s52, s52, 0x198000
	s_addc_u32 s53, s53, 0
	global_store_short v5, v146, s[52:53]
	s_add_u32 s52, s52, 0x198000
	s_addc_u32 s53, s53, 0
	global_store_short v5, v146, s[52:53]
	s_add_u32 s52, s52, 0x198000
	s_addc_u32 s53, s53, 0
	global_store_short v5, v146, s[52:53]
	s_add_u32 s52, s52, 0x198000
	s_addc_u32 s53, s53, 0
	global_store_short v5, v146, s[52:53]
	s_add_u32 s52, s52, 0x198000
	s_addc_u32 s53, s53, 0
	global_store_short v5, v146, s[52:53]
	s_add_u32 s52, s52, 0x198000
	s_addc_u32 s53, s53, 0
	global_store_short v5, v146, s[52:53]
	s_add_u32 s52, s52, 0x198000
	s_addc_u32 s53, s53, 0
	global_store_short v5, v146, s[52:53]
	s_mul_i32 s29, s27, 9
	s_add_u32 s26, s26, s29
	s_cmp_lt_u32 s26, 0x4400
	s_cbranch_scc1 .Lp3_chunk
.Lp3_end:
.LBB0_409:
	s_or_b64 exec, exec, s[16:17]
	s_waitcnt vmcnt(0)
	s_barrier
	s_and_saveexec_b64 s[4:5], s[40:41]
	s_cbranch_execz .LBB0_461
	s_add_i32 s3, 0, 0x27ff0
	v_mov_b32_e32 v1, s3
	s_waitcnt vmcnt(0) expcnt(0) lgkmcnt(0)
	ds_read_b32 v3, v1
	s_add_i32 s3, 0, 0x27ff4
	v_mov_b32_e32 v1, s3
	ds_read_b32 v1, v1
	s_waitcnt lgkmcnt(1)
	v_cmp_ne_u32_e32 vcc, 0, v3
	s_cbranch_vccnz .LBB0_425
	s_load_dwordx2 s[10:11], s[48:49], 0x4
	s_add_u32 s6, s42, 0x1000
	s_addc_u32 s7, s43, 0
	s_add_u32 s8, s42, 0x1100
	s_addc_u32 s9, s43, 0
	s_waitcnt lgkmcnt(0)
	s_mul_i32 s3, s10, s33
	s_add_u32 s10, s42, 0x1200
	s_mul_i32 s3, s3, s11
	s_addc_u32 s11, s43, 0
	s_add_u32 s12, s42, 0x1300
	s_addc_u32 s13, s43, 0
	s_mov_b32 s20, 1
	v_mov_b32_e32 v17, 0
	s_branch .LBB0_413
